# router bisection: four independent v_cmp_e64 into separate SGPR pairs before the popcounts (shorter VALU->SALU chain); compress GEMM1 gelu epilogue: 2/(e+1) by v_rcp_f32 + doubling instead of the IEEE
# speedup vs baseline: 1.0076x; 1.0001x over previous
.LBB0_1185:
	s_lshl_b32 s0, s30, 9
	s_and_b32 s0, s0, 0x400
	s_mov_b32 s1, s11
	v_lshl_add_u64 v[152:153], v[144:145], 0, s[0:1]
	global_load_dwordx4 v[84:87], v[152:153], off offset:16
	global_load_dwordx4 v[88:91], v[152:153], off
	v_lshl_add_u32 v154, s30, 8, v157
	s_waitcnt vmcnt(0)
	v_pk_add_f32 v[132:133], v[132:133], v[84:85]
	v_pk_add_f32 v[136:137], v[136:137], v[88:89]
	v_pk_add_f32 v[138:139], v[138:139], v[90:91]
	v_mul_f32_e32 v155, 0x3d372713, v136
	v_mul_f32_e32 v155, v136, v155
	v_fma_f32 v155, v136, v155, v136
	v_mul_f32_e32 v155, 0x3f4c422a, v155
	v_add_f32_e32 v155, v155, v155
	v_mul_f32_e32 v155, 0x3fb8aa3b, v155
	v_exp_f32_e32 v155, v155
	v_mul_f32_e32 v136, 0.5, v136
	v_pk_add_f32 v[134:135], v[134:135], v[86:87]
	v_pk_add_f32 v[128:129], v[128:129], v[88:89]
	v_add_f32_e32 v155, 1.0, v155
	v_pk_add_f32 v[124:125], v[124:125], v[84:85]
	v_pk_add_f32 v[130:131], v[130:131], v[90:91]
	v_pk_add_f32 v[126:127], v[126:127], v[86:87]
	v_rcp_f32_e32 v155, v155
	s_nop 0
	v_add_f32_e32 v155, v155, v155
	v_sub_f32_e32 v155, 1.0, v155
	v_add_f32_e32 v155, 1.0, v155
	v_mul_f32_e32 v136, v136, v155
	v_mul_f32_e32 v155, 0x3d372713, v132
	v_mul_f32_e32 v155, v132, v155
	v_fma_f32 v155, v132, v155, v132
	v_mul_f32_e32 v155, 0x3f4c422a, v155
	v_add_f32_e32 v155, v155, v155
	v_mul_f32_e32 v155, 0x3fb8aa3b, v155
	v_exp_f32_e32 v155, v155
	v_mul_f32_e32 v132, 0.5, v132
	v_pk_add_f32 v[120:121], v[120:121], v[88:89]
	v_pk_add_f32 v[116:117], v[116:117], v[84:85]
	v_add_f32_e32 v155, 1.0, v155
	v_pk_add_f32 v[122:123], v[122:123], v[90:91]
	v_pk_add_f32 v[118:119], v[118:119], v[86:87]
	v_pk_add_f32 v[112:113], v[112:113], v[88:89]
	v_rcp_f32_e32 v155, v155
	s_nop 0
	v_add_f32_e32 v155, v155, v155
	v_sub_f32_e32 v155, 1.0, v155
	v_add_f32_e32 v155, 1.0, v155
	v_mul_f32_e32 v132, v132, v155
	v_mul_f32_e32 v155, 0x3d372713, v137
	v_mul_f32_e32 v155, v137, v155
	v_fma_f32 v155, v137, v155, v137
	v_mul_f32_e32 v155, 0x3f4c422a, v155
	v_add_f32_e32 v155, v155, v155
	v_mul_f32_e32 v155, 0x3fb8aa3b, v155
	v_exp_f32_e32 v155, v155
	v_mul_f32_e32 v137, 0.5, v137
	v_pk_add_f32 v[108:109], v[108:109], v[84:85]
	v_pk_add_f32 v[114:115], v[114:115], v[90:91]
	v_add_f32_e32 v155, 1.0, v155
	v_pk_add_f32 v[110:111], v[110:111], v[86:87]
	v_pk_add_f32 v[104:105], v[104:105], v[88:89]
	v_pk_add_f32 v[100:101], v[100:101], v[84:85]
	v_rcp_f32_e32 v155, v155
	s_nop 0
	v_add_f32_e32 v155, v155, v155
	v_sub_f32_e32 v155, 1.0, v155
	v_add_f32_e32 v155, 1.0, v155
	v_mul_f32_e32 v137, v137, v155
	v_mul_f32_e32 v155, 0x3d372713, v133
	v_mul_f32_e32 v155, v133, v155
	v_fma_f32 v155, v133, v155, v133
	v_mul_f32_e32 v155, 0x3f4c422a, v155
	v_add_f32_e32 v155, v155, v155
	v_mul_f32_e32 v155, 0x3fb8aa3b, v155
	v_exp_f32_e32 v155, v155
	v_mul_f32_e32 v133, 0.5, v133
	v_pk_add_f32 v[106:107], v[106:107], v[90:91]
	v_pk_add_f32 v[102:103], v[102:103], v[86:87]
	v_add_f32_e32 v155, 1.0, v155
	v_pk_add_f32 v[96:97], v[96:97], v[88:89]
	v_pk_add_f32 v[92:93], v[92:93], v[84:85]
	v_pk_add_f32 v[98:99], v[98:99], v[90:91]
	v_rcp_f32_e32 v155, v155
	s_nop 0
	v_add_f32_e32 v155, v155, v155
	v_sub_f32_e32 v155, 1.0, v155
	v_add_f32_e32 v155, 1.0, v155
	v_mul_f32_e32 v133, v133, v155
	v_mul_f32_e32 v155, 0x3d372713, v138
	v_mul_f32_e32 v155, v138, v155
	v_fma_f32 v155, v138, v155, v138
	v_mul_f32_e32 v155, 0x3f4c422a, v155
	v_add_f32_e32 v155, v155, v155
	v_mul_f32_e32 v155, 0x3fb8aa3b, v155
	v_exp_f32_e32 v155, v155
	v_mul_f32_e32 v138, 0.5, v138
	v_pk_add_f32 v[94:95], v[94:95], v[86:87]
	v_pk_add_f32 v[80:81], v[80:81], v[88:89]
	v_add_f32_e32 v155, 1.0, v155
	v_pk_add_f32 v[76:77], v[76:77], v[84:85]
	v_pk_add_f32 v[82:83], v[82:83], v[90:91]
	v_pk_add_f32 v[78:79], v[78:79], v[86:87]
	v_rcp_f32_e32 v155, v155
	s_nop 0
	v_add_f32_e32 v155, v155, v155
	v_sub_f32_e32 v155, 1.0, v155
	v_add_f32_e32 v155, 1.0, v155
	v_mul_f32_e32 v138, v138, v155
	v_mul_f32_e32 v155, 0x3d372713, v134
	v_mul_f32_e32 v155, v134, v155
	v_fma_f32 v155, v134, v155, v134
	v_mul_f32_e32 v155, 0x3f4c422a, v155
	v_add_f32_e32 v155, v155, v155
	v_mul_f32_e32 v155, 0x3fb8aa3b, v155
	v_exp_f32_e32 v155, v155
	v_mul_f32_e32 v134, 0.5, v134
	v_pk_add_f32 v[72:73], v[72:73], v[88:89]
	v_pk_add_f32 v[68:69], v[68:69], v[84:85]
	v_add_f32_e32 v155, 1.0, v155
	v_pk_add_f32 v[74:75], v[74:75], v[90:91]
	v_pk_add_f32 v[70:71], v[70:71], v[86:87]
	v_rcp_f32_e32 v155, v155
	s_nop 0
	v_add_f32_e32 v155, v155, v155
	v_sub_f32_e32 v155, 1.0, v155
	v_add_f32_e32 v155, 1.0, v155
	v_mul_f32_e32 v155, v134, v155
	v_mul_f32_e32 v134, 0x3d372713, v139
	v_mul_f32_e32 v134, v139, v134
	v_fma_f32 v134, v139, v134, v139
	v_mul_f32_e32 v134, 0x3f4c422a, v134
	v_add_f32_e32 v134, v134, v134
	v_mul_f32_e32 v134, 0x3fb8aa3b, v134
	v_exp_f32_e32 v134, v134
	v_mul_f32_e32 v139, 0.5, v139
	v_add_f32_e32 v134, 1.0, v134
	v_rcp_f32_e32 v134, v134
	s_nop 0
	v_add_f32_e32 v134, v134, v134
	v_sub_f32_e32 v134, 1.0, v134
	v_add_f32_e32 v134, 1.0, v134
	v_mul_f32_e32 v139, v139, v134
	v_mul_f32_e32 v134, 0x3d372713, v135
	v_mul_f32_e32 v134, v135, v134
	v_fma_f32 v134, v135, v134, v135
	v_mul_f32_e32 v134, 0x3f4c422a, v134
	v_add_f32_e32 v134, v134, v134
	v_mul_f32_e32 v134, 0x3fb8aa3b, v134
	v_exp_f32_e32 v134, v134
	v_mul_f32_e32 v135, 0.5, v135
	v_add_f32_e32 v134, 1.0, v134
	v_rcp_f32_e32 v134, v134
	s_nop 0
	v_add_f32_e32 v134, v134, v134
	v_sub_f32_e32 v134, 1.0, v134
	v_add_f32_e32 v134, 1.0, v134
	v_mul_f32_e32 v160, v135, v134
	v_cvt_pk_bf16_f32 v134, v136, v137
	v_cvt_pk_bf16_f32 v135, v138, v139
	v_cvt_pk_bf16_f32 v136, v132, v133
	v_cvt_pk_bf16_f32 v137, v155, v160
	v_ashrrev_i32_e32 v155, 31, v154
	v_lshlrev_b64 v[132:133], 9, v[154:155]
	v_lshl_add_u64 v[132:133], v[146:147], 0, v[132:133]
	global_store_dwordx4 v[132:133], v[134:137], off
	s_nop 1
	v_mul_f32_e32 v134, 0x3d372713, v128
	v_mul_f32_e32 v134, v128, v134
	v_fma_f32 v134, v128, v134, v128
	v_mul_f32_e32 v134, 0x3f4c422a, v134
	v_add_f32_e32 v134, v134, v134
	v_mul_f32_e32 v134, 0x3fb8aa3b, v134
	v_exp_f32_e32 v134, v134
	v_mul_f32_e32 v128, 0.5, v128
	v_add_f32_e32 v134, 1.0, v134
	v_rcp_f32_e32 v134, v134
	s_nop 0
	v_add_f32_e32 v134, v134, v134
	v_sub_f32_e32 v134, 1.0, v134
	v_add_f32_e32 v134, 1.0, v134
	v_mul_f32_e32 v128, v128, v134
	v_mul_f32_e32 v134, 0x3d372713, v124
	v_mul_f32_e32 v134, v124, v134
	v_fma_f32 v134, v124, v134, v124
	v_mul_f32_e32 v134, 0x3f4c422a, v134
	v_add_f32_e32 v134, v134, v134
	v_mul_f32_e32 v134, 0x3fb8aa3b, v134
	v_exp_f32_e32 v134, v134
	v_mul_f32_e32 v124, 0.5, v124
	v_add_f32_e32 v134, 1.0, v134
	v_rcp_f32_e32 v134, v134
	s_nop 0
	v_add_f32_e32 v134, v134, v134
	v_sub_f32_e32 v134, 1.0, v134
	v_add_f32_e32 v134, 1.0, v134
	v_mul_f32_e32 v124, v124, v134
	v_mul_f32_e32 v134, 0x3d372713, v129
	v_mul_f32_e32 v134, v129, v134
	v_fma_f32 v134, v129, v134, v129
	v_mul_f32_e32 v134, 0x3f4c422a, v134
	v_add_f32_e32 v134, v134, v134
	v_mul_f32_e32 v134, 0x3fb8aa3b, v134
	v_exp_f32_e32 v134, v134
	v_mul_f32_e32 v129, 0.5, v129
	v_add_f32_e32 v134, 1.0, v134
	v_rcp_f32_e32 v134, v134
	s_nop 0
	v_add_f32_e32 v134, v134, v134
	v_sub_f32_e32 v134, 1.0, v134
	v_add_f32_e32 v134, 1.0, v134
	v_mul_f32_e32 v129, v129, v134
	v_mul_f32_e32 v134, 0x3d372713, v125
	v_mul_f32_e32 v134, v125, v134
	v_fma_f32 v134, v125, v134, v125
	v_mul_f32_e32 v134, 0x3f4c422a, v134
	v_add_f32_e32 v134, v134, v134
	v_mul_f32_e32 v134, 0x3fb8aa3b, v134
	v_exp_f32_e32 v134, v134
	v_mul_f32_e32 v125, 0.5, v125
	v_add_f32_e32 v134, 1.0, v134
	v_rcp_f32_e32 v134, v134
	s_nop 0
	v_add_f32_e32 v134, v134, v134
	v_sub_f32_e32 v134, 1.0, v134
	v_add_f32_e32 v134, 1.0, v134
	v_mul_f32_e32 v125, v125, v134
	v_mul_f32_e32 v134, 0x3d372713, v130
	v_mul_f32_e32 v134, v130, v134
	v_fma_f32 v134, v130, v134, v130
	v_mul_f32_e32 v134, 0x3f4c422a, v134
	v_add_f32_e32 v134, v134, v134
	v_mul_f32_e32 v134, 0x3fb8aa3b, v134
	v_exp_f32_e32 v134, v134
	v_mul_f32_e32 v130, 0.5, v130
	v_add_f32_e32 v134, 1.0, v134
	v_rcp_f32_e32 v134, v134
	s_nop 0
	v_add_f32_e32 v134, v134, v134
	v_sub_f32_e32 v134, 1.0, v134
	v_add_f32_e32 v134, 1.0, v134
	v_mul_f32_e32 v130, v130, v134
	v_mul_f32_e32 v134, 0x3d372713, v126
	v_mul_f32_e32 v134, v126, v134
	v_fma_f32 v134, v126, v134, v126
	v_mul_f32_e32 v134, 0x3f4c422a, v134
	v_add_f32_e32 v134, v134, v134
	v_mul_f32_e32 v134, 0x3fb8aa3b, v134
	v_exp_f32_e32 v134, v134
	v_mul_f32_e32 v126, 0.5, v126
	v_add_f32_e32 v134, 1.0, v134
	v_rcp_f32_e32 v134, v134
	s_nop 0
	v_add_f32_e32 v134, v134, v134
	v_sub_f32_e32 v134, 1.0, v134
	v_add_f32_e32 v134, 1.0, v134
	v_mul_f32_e32 v134, v126, v134
	v_mul_f32_e32 v126, 0x3d372713, v131
	v_mul_f32_e32 v126, v131, v126
	v_fma_f32 v126, v131, v126, v131
	v_mul_f32_e32 v126, 0x3f4c422a, v126
	v_add_f32_e32 v126, v126, v126
	v_mul_f32_e32 v126, 0x3fb8aa3b, v126
	v_exp_f32_e32 v126, v126
	v_mul_f32_e32 v131, 0.5, v131
	v_add_f32_e32 v126, 1.0, v126
	v_rcp_f32_e32 v126, v126
	s_nop 0
	v_add_f32_e32 v126, v126, v126
	v_sub_f32_e32 v126, 1.0, v126
	v_add_f32_e32 v126, 1.0, v126
	v_mul_f32_e32 v131, v131, v126
	v_mul_f32_e32 v126, 0x3d372713, v127
	v_mul_f32_e32 v126, v127, v126
	v_fma_f32 v126, v127, v126, v127
	v_mul_f32_e32 v126, 0x3f4c422a, v126
	v_add_f32_e32 v126, v126, v126
	v_mul_f32_e32 v126, 0x3fb8aa3b, v126
	v_exp_f32_e32 v126, v126
	v_mul_f32_e32 v127, 0.5, v127
	v_add_f32_e32 v126, 1.0, v126
	v_rcp_f32_e32 v126, v126
	s_nop 0
	v_add_f32_e32 v126, v126, v126
	v_sub_f32_e32 v126, 1.0, v126
	v_add_f32_e32 v126, 1.0, v126
	v_mul_f32_e32 v135, v127, v126
	v_cvt_pk_bf16_f32 v126, v128, v129
	v_cvt_pk_bf16_f32 v127, v130, v131
	v_cvt_pk_bf16_f32 v128, v124, v125
	v_or_b32_e32 v124, 16, v154
	v_ashrrev_i32_e32 v125, 31, v124
	v_lshlrev_b64 v[124:125], 9, v[124:125]
	v_lshl_add_u64 v[124:125], v[146:147], 0, v[124:125]
	v_cvt_pk_bf16_f32 v129, v134, v135
	global_store_dwordx4 v[124:125], v[126:129], off
	s_nop 1
	v_mul_f32_e32 v126, 0x3d372713, v120
	v_mul_f32_e32 v126, v120, v126
	v_fma_f32 v126, v120, v126, v120
	v_mul_f32_e32 v126, 0x3f4c422a, v126
	v_add_f32_e32 v126, v126, v126
	v_mul_f32_e32 v126, 0x3fb8aa3b, v126
	v_exp_f32_e32 v126, v126
	v_mul_f32_e32 v120, 0.5, v120
	v_add_f32_e32 v126, 1.0, v126
	v_rcp_f32_e32 v126, v126
	s_nop 0
	v_add_f32_e32 v126, v126, v126
	v_sub_f32_e32 v126, 1.0, v126
	v_add_f32_e32 v126, 1.0, v126
	v_mul_f32_e32 v120, v120, v126
	v_mul_f32_e32 v126, 0x3d372713, v116
	v_mul_f32_e32 v126, v116, v126
	v_fma_f32 v126, v116, v126, v116
	v_mul_f32_e32 v126, 0x3f4c422a, v126
	v_add_f32_e32 v126, v126, v126
	v_mul_f32_e32 v126, 0x3fb8aa3b, v126
	v_exp_f32_e32 v126, v126
	v_mul_f32_e32 v116, 0.5, v116
	v_add_f32_e32 v126, 1.0, v126
	v_rcp_f32_e32 v126, v126
	s_nop 0
	v_add_f32_e32 v126, v126, v126
	v_sub_f32_e32 v126, 1.0, v126
	v_add_f32_e32 v126, 1.0, v126
	v_mul_f32_e32 v116, v116, v126
	v_mul_f32_e32 v126, 0x3d372713, v121
	v_mul_f32_e32 v126, v121, v126
	v_fma_f32 v126, v121, v126, v121
	v_mul_f32_e32 v126, 0x3f4c422a, v126
	v_add_f32_e32 v126, v126, v126
	v_mul_f32_e32 v126, 0x3fb8aa3b, v126
	v_exp_f32_e32 v126, v126
	v_mul_f32_e32 v121, 0.5, v121
	v_add_f32_e32 v126, 1.0, v126
	v_rcp_f32_e32 v126, v126
	s_nop 0
	v_add_f32_e32 v126, v126, v126
	v_sub_f32_e32 v126, 1.0, v126
	v_add_f32_e32 v126, 1.0, v126
	v_mul_f32_e32 v121, v121, v126
	v_mul_f32_e32 v126, 0x3d372713, v117
	v_mul_f32_e32 v126, v117, v126
	v_fma_f32 v126, v117, v126, v117
	v_mul_f32_e32 v126, 0x3f4c422a, v126
	v_add_f32_e32 v126, v126, v126
	v_mul_f32_e32 v126, 0x3fb8aa3b, v126
	v_exp_f32_e32 v126, v126
	v_mul_f32_e32 v117, 0.5, v117
	v_add_f32_e32 v126, 1.0, v126
	v_rcp_f32_e32 v126, v126
	s_nop 0
	v_add_f32_e32 v126, v126, v126
	v_sub_f32_e32 v126, 1.0, v126
	v_add_f32_e32 v126, 1.0, v126
	v_mul_f32_e32 v117, v117, v126
	v_mul_f32_e32 v126, 0x3d372713, v122
	v_mul_f32_e32 v126, v122, v126
	v_fma_f32 v126, v122, v126, v122
	v_mul_f32_e32 v126, 0x3f4c422a, v126
	v_add_f32_e32 v126, v126, v126
	v_mul_f32_e32 v126, 0x3fb8aa3b, v126
	v_exp_f32_e32 v126, v126
	v_mul_f32_e32 v122, 0.5, v122
	v_add_f32_e32 v126, 1.0, v126
	v_rcp_f32_e32 v126, v126
	s_nop 0
	v_add_f32_e32 v126, v126, v126
	v_sub_f32_e32 v126, 1.0, v126
	v_add_f32_e32 v126, 1.0, v126
	v_mul_f32_e32 v122, v122, v126
	v_mul_f32_e32 v126, 0x3d372713, v118
	v_mul_f32_e32 v126, v118, v126
	v_fma_f32 v126, v118, v126, v118
	v_mul_f32_e32 v126, 0x3f4c422a, v126
	v_add_f32_e32 v126, v126, v126
	v_mul_f32_e32 v126, 0x3fb8aa3b, v126
	v_exp_f32_e32 v126, v126
	v_mul_f32_e32 v118, 0.5, v118
	v_add_f32_e32 v126, 1.0, v126
	v_rcp_f32_e32 v126, v126
	s_nop 0
	v_add_f32_e32 v126, v126, v126
	v_sub_f32_e32 v126, 1.0, v126
	v_add_f32_e32 v126, 1.0, v126
	v_mul_f32_e32 v126, v118, v126
	v_mul_f32_e32 v118, 0x3d372713, v123
	v_mul_f32_e32 v118, v123, v118
	v_fma_f32 v118, v123, v118, v123
	v_mul_f32_e32 v118, 0x3f4c422a, v118
	v_add_f32_e32 v118, v118, v118
	v_mul_f32_e32 v118, 0x3fb8aa3b, v118
	v_exp_f32_e32 v118, v118
	v_mul_f32_e32 v123, 0.5, v123
	v_add_f32_e32 v118, 1.0, v118
	v_rcp_f32_e32 v118, v118
	s_nop 0
	v_add_f32_e32 v118, v118, v118
	v_sub_f32_e32 v118, 1.0, v118
	v_add_f32_e32 v118, 1.0, v118
	v_mul_f32_e32 v123, v123, v118
	v_mul_f32_e32 v118, 0x3d372713, v119
	v_mul_f32_e32 v118, v119, v118
	v_fma_f32 v118, v119, v118, v119
	v_mul_f32_e32 v118, 0x3f4c422a, v118
	v_add_f32_e32 v118, v118, v118
	v_mul_f32_e32 v118, 0x3fb8aa3b, v118
	v_exp_f32_e32 v118, v118
	v_mul_f32_e32 v119, 0.5, v119
	v_add_f32_e32 v118, 1.0, v118
	v_rcp_f32_e32 v118, v118
	s_nop 0
	v_add_f32_e32 v118, v118, v118
	v_sub_f32_e32 v118, 1.0, v118
	v_add_f32_e32 v118, 1.0, v118
	v_mul_f32_e32 v127, v119, v118
	v_cvt_pk_bf16_f32 v118, v120, v121
	v_cvt_pk_bf16_f32 v119, v122, v123
	v_cvt_pk_bf16_f32 v120, v116, v117
	v_or_b32_e32 v116, 32, v154
	v_ashrrev_i32_e32 v117, 31, v116
	v_lshlrev_b64 v[116:117], 9, v[116:117]
	v_lshl_add_u64 v[116:117], v[146:147], 0, v[116:117]
	v_cvt_pk_bf16_f32 v121, v126, v127
	global_store_dwordx4 v[116:117], v[118:121], off
	s_nop 1
	v_mul_f32_e32 v118, 0x3d372713, v112
	v_mul_f32_e32 v118, v112, v118
	v_fma_f32 v118, v112, v118, v112
	v_mul_f32_e32 v118, 0x3f4c422a, v118
	v_add_f32_e32 v118, v118, v118
	v_mul_f32_e32 v118, 0x3fb8aa3b, v118
	v_exp_f32_e32 v118, v118
	v_mul_f32_e32 v112, 0.5, v112
	v_add_f32_e32 v118, 1.0, v118
	v_rcp_f32_e32 v118, v118
	s_nop 0
	v_add_f32_e32 v118, v118, v118
	v_sub_f32_e32 v118, 1.0, v118
	v_add_f32_e32 v118, 1.0, v118
	v_mul_f32_e32 v112, v112, v118
	v_mul_f32_e32 v118, 0x3d372713, v108
	v_mul_f32_e32 v118, v108, v118
	v_fma_f32 v118, v108, v118, v108
	v_mul_f32_e32 v118, 0x3f4c422a, v118
	v_add_f32_e32 v118, v118, v118
	v_mul_f32_e32 v118, 0x3fb8aa3b, v118
	v_exp_f32_e32 v118, v118
	v_mul_f32_e32 v108, 0.5, v108
	v_add_f32_e32 v118, 1.0, v118
	v_rcp_f32_e32 v118, v118
	s_nop 0
	v_add_f32_e32 v118, v118, v118
	v_sub_f32_e32 v118, 1.0, v118
	v_add_f32_e32 v118, 1.0, v118
	v_mul_f32_e32 v108, v108, v118
	v_mul_f32_e32 v118, 0x3d372713, v113
	v_mul_f32_e32 v118, v113, v118
	v_fma_f32 v118, v113, v118, v113
	v_mul_f32_e32 v118, 0x3f4c422a, v118
	v_add_f32_e32 v118, v118, v118
	v_mul_f32_e32 v118, 0x3fb8aa3b, v118
	v_exp_f32_e32 v118, v118
	v_mul_f32_e32 v113, 0.5, v113
	v_add_f32_e32 v118, 1.0, v118
	v_rcp_f32_e32 v118, v118
	s_nop 0
	v_add_f32_e32 v118, v118, v118
	v_sub_f32_e32 v118, 1.0, v118
	v_add_f32_e32 v118, 1.0, v118
	v_mul_f32_e32 v113, v113, v118
	v_mul_f32_e32 v118, 0x3d372713, v109
	v_mul_f32_e32 v118, v109, v118
	v_fma_f32 v118, v109, v118, v109
	v_mul_f32_e32 v118, 0x3f4c422a, v118
	v_add_f32_e32 v118, v118, v118
	v_mul_f32_e32 v118, 0x3fb8aa3b, v118
	v_exp_f32_e32 v118, v118
	v_mul_f32_e32 v109, 0.5, v109
	v_add_f32_e32 v118, 1.0, v118
	v_rcp_f32_e32 v118, v118
	s_nop 0
	v_add_f32_e32 v118, v118, v118
	v_sub_f32_e32 v118, 1.0, v118
	v_add_f32_e32 v118, 1.0, v118
	v_mul_f32_e32 v109, v109, v118
	v_mul_f32_e32 v118, 0x3d372713, v114
	v_mul_f32_e32 v118, v114, v118
	v_fma_f32 v118, v114, v118, v114
	v_mul_f32_e32 v118, 0x3f4c422a, v118
	v_add_f32_e32 v118, v118, v118
	v_mul_f32_e32 v118, 0x3fb8aa3b, v118
	v_exp_f32_e32 v118, v118
	v_mul_f32_e32 v114, 0.5, v114
	v_add_f32_e32 v118, 1.0, v118
	v_rcp_f32_e32 v118, v118
	s_nop 0
	v_add_f32_e32 v118, v118, v118
	v_sub_f32_e32 v118, 1.0, v118
	v_add_f32_e32 v118, 1.0, v118
	v_mul_f32_e32 v114, v114, v118
	v_mul_f32_e32 v118, 0x3d372713, v110
	v_mul_f32_e32 v118, v110, v118
	v_fma_f32 v118, v110, v118, v110
	v_mul_f32_e32 v118, 0x3f4c422a, v118
	v_add_f32_e32 v118, v118, v118
	v_mul_f32_e32 v118, 0x3fb8aa3b, v118
	v_exp_f32_e32 v118, v118
	v_mul_f32_e32 v110, 0.5, v110
	v_add_f32_e32 v118, 1.0, v118
	v_rcp_f32_e32 v118, v118
	s_nop 0
	v_add_f32_e32 v118, v118, v118
	v_sub_f32_e32 v118, 1.0, v118
	v_add_f32_e32 v118, 1.0, v118
	v_mul_f32_e32 v118, v110, v118
	v_mul_f32_e32 v110, 0x3d372713, v115
	v_mul_f32_e32 v110, v115, v110
	v_fma_f32 v110, v115, v110, v115
	v_mul_f32_e32 v110, 0x3f4c422a, v110
	v_add_f32_e32 v110, v110, v110
	v_mul_f32_e32 v110, 0x3fb8aa3b, v110
	v_exp_f32_e32 v110, v110
	v_mul_f32_e32 v115, 0.5, v115
	v_add_f32_e32 v110, 1.0, v110
	v_rcp_f32_e32 v110, v110
	s_nop 0
	v_add_f32_e32 v110, v110, v110
	v_sub_f32_e32 v110, 1.0, v110
	v_add_f32_e32 v110, 1.0, v110
	v_mul_f32_e32 v115, v115, v110
	v_mul_f32_e32 v110, 0x3d372713, v111
	v_mul_f32_e32 v110, v111, v110
	v_fma_f32 v110, v111, v110, v111
	v_mul_f32_e32 v110, 0x3f4c422a, v110
	v_add_f32_e32 v110, v110, v110
	v_mul_f32_e32 v110, 0x3fb8aa3b, v110
	v_exp_f32_e32 v110, v110
	v_mul_f32_e32 v111, 0.5, v111
	v_add_f32_e32 v110, 1.0, v110
	v_rcp_f32_e32 v110, v110
	s_nop 0
	v_add_f32_e32 v110, v110, v110
	v_sub_f32_e32 v110, 1.0, v110
	v_add_f32_e32 v110, 1.0, v110
	v_mul_f32_e32 v119, v111, v110
	v_cvt_pk_bf16_f32 v110, v112, v113
	v_cvt_pk_bf16_f32 v111, v114, v115
	v_cvt_pk_bf16_f32 v112, v108, v109
	v_or_b32_e32 v108, 48, v154
	v_ashrrev_i32_e32 v109, 31, v108
	v_lshlrev_b64 v[108:109], 9, v[108:109]
	v_lshl_add_u64 v[108:109], v[146:147], 0, v[108:109]
	v_cvt_pk_bf16_f32 v113, v118, v119
	global_store_dwordx4 v[108:109], v[110:113], off
	s_nop 1
	v_mul_f32_e32 v111, 0x3d372713, v104
	v_mul_f32_e32 v111, v104, v111
	v_fma_f32 v111, v104, v111, v104
	v_mul_f32_e32 v111, 0x3f4c422a, v111
	v_add_f32_e32 v111, v111, v111
	v_mul_f32_e32 v111, 0x3fb8aa3b, v111
	v_exp_f32_e32 v111, v111
	v_mul_f32_e32 v104, 0.5, v104
	v_add_u32_e32 v110, 0x80, v154
	v_add_f32_e32 v111, 1.0, v111
	v_rcp_f32_e32 v111, v111
	s_nop 0
	v_add_f32_e32 v111, v111, v111
	v_sub_f32_e32 v111, 1.0, v111
	v_add_f32_e32 v111, 1.0, v111
	v_mul_f32_e32 v104, v104, v111
	v_mul_f32_e32 v111, 0x3d372713, v100
	v_mul_f32_e32 v111, v100, v111
	v_fma_f32 v111, v100, v111, v100
	v_mul_f32_e32 v111, 0x3f4c422a, v111
	v_add_f32_e32 v111, v111, v111
	v_mul_f32_e32 v111, 0x3fb8aa3b, v111
	v_exp_f32_e32 v111, v111
	v_mul_f32_e32 v100, 0.5, v100
	v_add_f32_e32 v111, 1.0, v111
	v_rcp_f32_e32 v111, v111
	s_nop 0
	v_add_f32_e32 v111, v111, v111
	v_sub_f32_e32 v111, 1.0, v111
	v_add_f32_e32 v111, 1.0, v111
	v_mul_f32_e32 v100, v100, v111
	v_mul_f32_e32 v111, 0x3d372713, v105
	v_mul_f32_e32 v111, v105, v111
	v_fma_f32 v111, v105, v111, v105
	v_mul_f32_e32 v111, 0x3f4c422a, v111
	v_add_f32_e32 v111, v111, v111
	v_mul_f32_e32 v111, 0x3fb8aa3b, v111
	v_exp_f32_e32 v111, v111
	v_mul_f32_e32 v105, 0.5, v105
	v_add_f32_e32 v111, 1.0, v111
	v_rcp_f32_e32 v111, v111
	s_nop 0
	v_add_f32_e32 v111, v111, v111
	v_sub_f32_e32 v111, 1.0, v111
	v_add_f32_e32 v111, 1.0, v111
	v_mul_f32_e32 v105, v105, v111
	v_mul_f32_e32 v111, 0x3d372713, v101
	v_mul_f32_e32 v111, v101, v111
	v_fma_f32 v111, v101, v111, v101
	v_mul_f32_e32 v111, 0x3f4c422a, v111
	v_add_f32_e32 v111, v111, v111
	v_mul_f32_e32 v111, 0x3fb8aa3b, v111
	v_exp_f32_e32 v111, v111
	v_mul_f32_e32 v101, 0.5, v101
	v_add_f32_e32 v111, 1.0, v111
	v_rcp_f32_e32 v111, v111
	s_nop 0
	v_add_f32_e32 v111, v111, v111
	v_sub_f32_e32 v111, 1.0, v111
	v_add_f32_e32 v111, 1.0, v111
	v_mul_f32_e32 v101, v101, v111
	v_mul_f32_e32 v111, 0x3d372713, v106
	v_mul_f32_e32 v111, v106, v111
	v_fma_f32 v111, v106, v111, v106
	v_mul_f32_e32 v111, 0x3f4c422a, v111
	v_add_f32_e32 v111, v111, v111
	v_mul_f32_e32 v111, 0x3fb8aa3b, v111
	v_exp_f32_e32 v111, v111
	v_mul_f32_e32 v106, 0.5, v106
	v_add_f32_e32 v111, 1.0, v111
	v_rcp_f32_e32 v111, v111
	s_nop 0
	v_add_f32_e32 v111, v111, v111
	v_sub_f32_e32 v111, 1.0, v111
	v_add_f32_e32 v111, 1.0, v111
	v_mul_f32_e32 v106, v106, v111
	v_mul_f32_e32 v111, 0x3d372713, v102
	v_mul_f32_e32 v111, v102, v111
	v_fma_f32 v111, v102, v111, v102
	v_mul_f32_e32 v111, 0x3f4c422a, v111
	v_add_f32_e32 v111, v111, v111
	v_mul_f32_e32 v111, 0x3fb8aa3b, v111
	v_exp_f32_e32 v111, v111
	v_mul_f32_e32 v102, 0.5, v102
	v_add_f32_e32 v111, 1.0, v111
	v_rcp_f32_e32 v111, v111
	s_nop 0
	v_add_f32_e32 v111, v111, v111
	v_sub_f32_e32 v111, 1.0, v111
	v_add_f32_e32 v111, 1.0, v111
	v_mul_f32_e32 v111, v102, v111
	v_mul_f32_e32 v102, 0x3d372713, v107
	v_mul_f32_e32 v102, v107, v102
	v_fma_f32 v102, v107, v102, v107
	v_mul_f32_e32 v102, 0x3f4c422a, v102
	v_add_f32_e32 v102, v102, v102
	v_mul_f32_e32 v102, 0x3fb8aa3b, v102
	v_exp_f32_e32 v102, v102
	v_mul_f32_e32 v107, 0.5, v107
	v_add_f32_e32 v102, 1.0, v102
	v_rcp_f32_e32 v102, v102
	s_nop 0
	v_add_f32_e32 v102, v102, v102
	v_sub_f32_e32 v102, 1.0, v102
	v_add_f32_e32 v102, 1.0, v102
	v_mul_f32_e32 v107, v107, v102
	v_mul_f32_e32 v102, 0x3d372713, v103
	v_mul_f32_e32 v102, v103, v102
	v_fma_f32 v102, v103, v102, v103
	v_mul_f32_e32 v102, 0x3f4c422a, v102
	v_add_f32_e32 v102, v102, v102
	v_mul_f32_e32 v102, 0x3fb8aa3b, v102
	v_exp_f32_e32 v102, v102
	v_mul_f32_e32 v103, 0.5, v103
	v_add_f32_e32 v102, 1.0, v102
	v_rcp_f32_e32 v102, v102
	s_nop 0
	v_add_f32_e32 v102, v102, v102
	v_sub_f32_e32 v102, 1.0, v102
	v_add_f32_e32 v102, 1.0, v102
	v_mul_f32_e32 v112, v103, v102
	v_cvt_pk_bf16_f32 v102, v104, v105
	v_cvt_pk_bf16_f32 v103, v106, v107
	v_cvt_pk_bf16_f32 v104, v100, v101
	v_cvt_pk_bf16_f32 v105, v111, v112
	v_ashrrev_i32_e32 v111, 31, v110
	v_lshlrev_b64 v[100:101], 9, v[110:111]
	v_lshl_add_u64 v[100:101], v[146:147], 0, v[100:101]
	global_store_dwordx4 v[100:101], v[102:105], off
	s_nop 1
	v_mul_f32_e32 v102, 0x3d372713, v96
	v_mul_f32_e32 v102, v96, v102
	v_fma_f32 v102, v96, v102, v96
	v_mul_f32_e32 v102, 0x3f4c422a, v102
	v_add_f32_e32 v102, v102, v102
	v_mul_f32_e32 v102, 0x3fb8aa3b, v102
	v_exp_f32_e32 v102, v102
	v_mul_f32_e32 v96, 0.5, v96
	v_add_f32_e32 v102, 1.0, v102
	v_rcp_f32_e32 v102, v102
	s_nop 0
	v_add_f32_e32 v102, v102, v102
	v_sub_f32_e32 v102, 1.0, v102
	v_add_f32_e32 v102, 1.0, v102
	v_mul_f32_e32 v96, v96, v102
	v_mul_f32_e32 v102, 0x3d372713, v92
	v_mul_f32_e32 v102, v92, v102
	v_fma_f32 v102, v92, v102, v92
	v_mul_f32_e32 v102, 0x3f4c422a, v102
	v_add_f32_e32 v102, v102, v102
	v_mul_f32_e32 v102, 0x3fb8aa3b, v102
	v_exp_f32_e32 v102, v102
	v_mul_f32_e32 v92, 0.5, v92
	v_add_f32_e32 v102, 1.0, v102
	v_rcp_f32_e32 v102, v102
	s_nop 0
	v_add_f32_e32 v102, v102, v102
	v_sub_f32_e32 v102, 1.0, v102
	v_add_f32_e32 v102, 1.0, v102
	v_mul_f32_e32 v92, v92, v102
	v_mul_f32_e32 v102, 0x3d372713, v97
	v_mul_f32_e32 v102, v97, v102
	v_fma_f32 v102, v97, v102, v97
	v_mul_f32_e32 v102, 0x3f4c422a, v102
	v_add_f32_e32 v102, v102, v102
	v_mul_f32_e32 v102, 0x3fb8aa3b, v102
	v_exp_f32_e32 v102, v102
	v_mul_f32_e32 v97, 0.5, v97
	v_add_f32_e32 v102, 1.0, v102
	v_rcp_f32_e32 v102, v102
	s_nop 0
	v_add_f32_e32 v102, v102, v102
	v_sub_f32_e32 v102, 1.0, v102
	v_add_f32_e32 v102, 1.0, v102
	v_mul_f32_e32 v97, v97, v102
	v_mul_f32_e32 v102, 0x3d372713, v93
	v_mul_f32_e32 v102, v93, v102
	v_fma_f32 v102, v93, v102, v93
	v_mul_f32_e32 v102, 0x3f4c422a, v102
	v_add_f32_e32 v102, v102, v102
	v_mul_f32_e32 v102, 0x3fb8aa3b, v102
	v_exp_f32_e32 v102, v102
	v_mul_f32_e32 v93, 0.5, v93
	v_add_f32_e32 v102, 1.0, v102
	v_rcp_f32_e32 v102, v102
	s_nop 0
	v_add_f32_e32 v102, v102, v102
	v_sub_f32_e32 v102, 1.0, v102
	v_add_f32_e32 v102, 1.0, v102
	v_mul_f32_e32 v93, v93, v102
	v_mul_f32_e32 v102, 0x3d372713, v98
	v_mul_f32_e32 v102, v98, v102
	v_fma_f32 v102, v98, v102, v98
	v_mul_f32_e32 v102, 0x3f4c422a, v102
	v_add_f32_e32 v102, v102, v102
	v_mul_f32_e32 v102, 0x3fb8aa3b, v102
	v_exp_f32_e32 v102, v102
	v_mul_f32_e32 v98, 0.5, v98
	v_add_f32_e32 v102, 1.0, v102
	v_rcp_f32_e32 v102, v102
	s_nop 0
	v_add_f32_e32 v102, v102, v102
	v_sub_f32_e32 v102, 1.0, v102
	v_add_f32_e32 v102, 1.0, v102
	v_mul_f32_e32 v98, v98, v102
	v_mul_f32_e32 v102, 0x3d372713, v94
	v_mul_f32_e32 v102, v94, v102
	v_fma_f32 v102, v94, v102, v94
	v_mul_f32_e32 v102, 0x3f4c422a, v102
	v_add_f32_e32 v102, v102, v102
	v_mul_f32_e32 v102, 0x3fb8aa3b, v102
	v_exp_f32_e32 v102, v102
	v_mul_f32_e32 v94, 0.5, v94
	v_add_f32_e32 v102, 1.0, v102
	v_rcp_f32_e32 v102, v102
	s_nop 0
	v_add_f32_e32 v102, v102, v102
	v_sub_f32_e32 v102, 1.0, v102
	v_add_f32_e32 v102, 1.0, v102
	v_mul_f32_e32 v102, v94, v102
	v_mul_f32_e32 v94, 0x3d372713, v99
	v_mul_f32_e32 v94, v99, v94
	v_fma_f32 v94, v99, v94, v99
	v_mul_f32_e32 v94, 0x3f4c422a, v94
	v_add_f32_e32 v94, v94, v94
	v_mul_f32_e32 v94, 0x3fb8aa3b, v94
	v_exp_f32_e32 v94, v94
	v_mul_f32_e32 v99, 0.5, v99
	v_add_f32_e32 v94, 1.0, v94
	v_rcp_f32_e32 v94, v94
	s_nop 0
	v_add_f32_e32 v94, v94, v94
	v_sub_f32_e32 v94, 1.0, v94
	v_add_f32_e32 v94, 1.0, v94
	v_mul_f32_e32 v99, v99, v94
	v_mul_f32_e32 v94, 0x3d372713, v95
	v_mul_f32_e32 v94, v95, v94
	v_fma_f32 v94, v95, v94, v95
	v_mul_f32_e32 v94, 0x3f4c422a, v94
	v_add_f32_e32 v94, v94, v94
	v_mul_f32_e32 v94, 0x3fb8aa3b, v94
	v_exp_f32_e32 v94, v94
	v_mul_f32_e32 v95, 0.5, v95
	v_add_f32_e32 v94, 1.0, v94
	v_rcp_f32_e32 v94, v94
	s_nop 0
	v_add_f32_e32 v94, v94, v94
	v_sub_f32_e32 v94, 1.0, v94
	v_add_f32_e32 v94, 1.0, v94
	v_mul_f32_e32 v103, v95, v94
	v_cvt_pk_bf16_f32 v94, v96, v97
	v_cvt_pk_bf16_f32 v95, v98, v99
	v_cvt_pk_bf16_f32 v96, v92, v93
	v_add_u32_e32 v92, 0x90, v154
	v_ashrrev_i32_e32 v93, 31, v92
	v_lshlrev_b64 v[92:93], 9, v[92:93]
	v_lshl_add_u64 v[92:93], v[146:147], 0, v[92:93]
	v_cvt_pk_bf16_f32 v97, v102, v103
	global_store_dwordx4 v[92:93], v[94:97], off
	s_nop 1
	v_mul_f32_e32 v94, 0x3d372713, v80
	v_mul_f32_e32 v94, v80, v94
	v_fma_f32 v94, v80, v94, v80
	v_mul_f32_e32 v94, 0x3f4c422a, v94
	v_add_f32_e32 v94, v94, v94
	v_mul_f32_e32 v94, 0x3fb8aa3b, v94
	v_exp_f32_e32 v94, v94
	v_mul_f32_e32 v80, 0.5, v80
	v_add_f32_e32 v94, 1.0, v94
	v_rcp_f32_e32 v94, v94
	s_nop 0
	v_add_f32_e32 v94, v94, v94
	v_sub_f32_e32 v94, 1.0, v94
	v_add_f32_e32 v94, 1.0, v94
	v_mul_f32_e32 v80, v80, v94
	v_mul_f32_e32 v94, 0x3d372713, v76
	v_mul_f32_e32 v94, v76, v94
	v_fma_f32 v94, v76, v94, v76
	v_mul_f32_e32 v94, 0x3f4c422a, v94
	v_add_f32_e32 v94, v94, v94
	v_mul_f32_e32 v94, 0x3fb8aa3b, v94
	v_exp_f32_e32 v94, v94
	v_mul_f32_e32 v76, 0.5, v76
	v_add_f32_e32 v94, 1.0, v94
	v_rcp_f32_e32 v94, v94
	s_nop 0
	v_add_f32_e32 v94, v94, v94
	v_sub_f32_e32 v94, 1.0, v94
	v_add_f32_e32 v94, 1.0, v94
	v_mul_f32_e32 v76, v76, v94
	v_mul_f32_e32 v94, 0x3d372713, v81
	v_mul_f32_e32 v94, v81, v94
	v_fma_f32 v94, v81, v94, v81
	v_mul_f32_e32 v94, 0x3f4c422a, v94
	v_add_f32_e32 v94, v94, v94
	v_mul_f32_e32 v94, 0x3fb8aa3b, v94
	v_exp_f32_e32 v94, v94
	v_mul_f32_e32 v81, 0.5, v81
	v_add_f32_e32 v94, 1.0, v94
	v_rcp_f32_e32 v94, v94
	s_nop 0
	v_add_f32_e32 v94, v94, v94
	v_sub_f32_e32 v94, 1.0, v94
	v_add_f32_e32 v94, 1.0, v94
	v_mul_f32_e32 v81, v81, v94
	v_mul_f32_e32 v94, 0x3d372713, v77
	v_mul_f32_e32 v94, v77, v94
	v_fma_f32 v94, v77, v94, v77
	v_mul_f32_e32 v94, 0x3f4c422a, v94
	v_add_f32_e32 v94, v94, v94
	v_mul_f32_e32 v94, 0x3fb8aa3b, v94
	v_exp_f32_e32 v94, v94
	v_mul_f32_e32 v77, 0.5, v77
	v_add_f32_e32 v94, 1.0, v94
	v_rcp_f32_e32 v94, v94
	s_nop 0
	v_add_f32_e32 v94, v94, v94
	v_sub_f32_e32 v94, 1.0, v94
	v_add_f32_e32 v94, 1.0, v94
	v_mul_f32_e32 v77, v77, v94
	v_mul_f32_e32 v94, 0x3d372713, v82
	v_mul_f32_e32 v94, v82, v94
	v_fma_f32 v94, v82, v94, v82
	v_mul_f32_e32 v94, 0x3f4c422a, v94
	v_add_f32_e32 v94, v94, v94
	v_mul_f32_e32 v94, 0x3fb8aa3b, v94
	v_exp_f32_e32 v94, v94
	v_mul_f32_e32 v82, 0.5, v82
	v_add_f32_e32 v94, 1.0, v94
	v_rcp_f32_e32 v94, v94
	s_nop 0
	v_add_f32_e32 v94, v94, v94
	v_sub_f32_e32 v94, 1.0, v94
	v_add_f32_e32 v94, 1.0, v94
	v_mul_f32_e32 v82, v82, v94
	v_mul_f32_e32 v94, 0x3d372713, v78
	v_mul_f32_e32 v94, v78, v94
	v_fma_f32 v94, v78, v94, v78
	v_mul_f32_e32 v94, 0x3f4c422a, v94
	v_add_f32_e32 v94, v94, v94
	v_mul_f32_e32 v94, 0x3fb8aa3b, v94
	v_exp_f32_e32 v94, v94
	v_mul_f32_e32 v78, 0.5, v78
	v_add_f32_e32 v94, 1.0, v94
	v_rcp_f32_e32 v94, v94
	s_nop 0
	v_add_f32_e32 v94, v94, v94
	v_sub_f32_e32 v94, 1.0, v94
	v_add_f32_e32 v94, 1.0, v94
	v_mul_f32_e32 v94, v78, v94
	v_mul_f32_e32 v78, 0x3d372713, v83
	v_mul_f32_e32 v78, v83, v78
	v_fma_f32 v78, v83, v78, v83
	v_mul_f32_e32 v78, 0x3f4c422a, v78
	v_add_f32_e32 v78, v78, v78
	v_mul_f32_e32 v78, 0x3fb8aa3b, v78
	v_exp_f32_e32 v78, v78
	v_mul_f32_e32 v83, 0.5, v83
	v_add_f32_e32 v78, 1.0, v78
	v_rcp_f32_e32 v78, v78
	s_nop 0
	v_add_f32_e32 v78, v78, v78
	v_sub_f32_e32 v78, 1.0, v78
	v_add_f32_e32 v78, 1.0, v78
	v_mul_f32_e32 v83, v83, v78
	v_mul_f32_e32 v78, 0x3d372713, v79
	v_mul_f32_e32 v78, v79, v78
	v_fma_f32 v78, v79, v78, v79
	v_mul_f32_e32 v78, 0x3f4c422a, v78
	v_add_f32_e32 v78, v78, v78
	v_mul_f32_e32 v78, 0x3fb8aa3b, v78
	v_exp_f32_e32 v78, v78
	v_mul_f32_e32 v79, 0.5, v79
	v_add_f32_e32 v78, 1.0, v78
	v_rcp_f32_e32 v78, v78
	s_nop 0
	v_add_f32_e32 v78, v78, v78
	v_sub_f32_e32 v78, 1.0, v78
	v_add_f32_e32 v78, 1.0, v78
	v_mul_f32_e32 v95, v79, v78
	v_cvt_pk_bf16_f32 v78, v80, v81
	v_cvt_pk_bf16_f32 v79, v82, v83
	v_cvt_pk_bf16_f32 v80, v76, v77
	v_add_u32_e32 v76, 0xa0, v154
	v_ashrrev_i32_e32 v77, 31, v76
	v_lshlrev_b64 v[76:77], 9, v[76:77]
	v_lshl_add_u64 v[76:77], v[146:147], 0, v[76:77]
	v_cvt_pk_bf16_f32 v81, v94, v95
	global_store_dwordx4 v[76:77], v[78:81], off
	s_nop 1
	v_mul_f32_e32 v78, 0x3d372713, v72
	v_mul_f32_e32 v78, v72, v78
	v_fma_f32 v78, v72, v78, v72
	v_mul_f32_e32 v78, 0x3f4c422a, v78
	v_add_f32_e32 v78, v78, v78
	v_mul_f32_e32 v78, 0x3fb8aa3b, v78
	v_exp_f32_e32 v78, v78
	v_mul_f32_e32 v72, 0.5, v72
	v_add_f32_e32 v78, 1.0, v78
	v_rcp_f32_e32 v78, v78
	s_nop 0
	v_add_f32_e32 v78, v78, v78
	v_sub_f32_e32 v78, 1.0, v78
	v_add_f32_e32 v78, 1.0, v78
	v_mul_f32_e32 v72, v72, v78
	v_mul_f32_e32 v78, 0x3d372713, v68
	v_mul_f32_e32 v78, v68, v78
	v_fma_f32 v78, v68, v78, v68
	v_mul_f32_e32 v78, 0x3f4c422a, v78
	v_add_f32_e32 v78, v78, v78
	v_mul_f32_e32 v78, 0x3fb8aa3b, v78
	v_exp_f32_e32 v78, v78
	v_mul_f32_e32 v68, 0.5, v68
	v_add_f32_e32 v78, 1.0, v78
	v_rcp_f32_e32 v78, v78
	s_nop 0
	v_add_f32_e32 v78, v78, v78
	v_sub_f32_e32 v78, 1.0, v78
	v_add_f32_e32 v78, 1.0, v78
	v_mul_f32_e32 v78, v68, v78
	v_mul_f32_e32 v68, 0x3d372713, v73
	v_mul_f32_e32 v68, v73, v68
	v_fma_f32 v68, v73, v68, v73
	v_mul_f32_e32 v68, 0x3f4c422a, v68
	v_add_f32_e32 v68, v68, v68
	v_mul_f32_e32 v68, 0x3fb8aa3b, v68
	v_exp_f32_e32 v68, v68
	v_mul_f32_e32 v73, 0.5, v73
	v_add_f32_e32 v68, 1.0, v68
	v_rcp_f32_e32 v68, v68
	s_nop 0
	v_add_f32_e32 v68, v68, v68
	v_sub_f32_e32 v68, 1.0, v68
	v_add_f32_e32 v68, 1.0, v68
	v_mul_f32_e32 v68, v73, v68
	v_mul_f32_e32 v73, 0x3d372713, v69
	v_mul_f32_e32 v73, v69, v73
	v_fma_f32 v73, v69, v73, v69
	v_mul_f32_e32 v73, 0x3f4c422a, v73
	v_add_f32_e32 v73, v73, v73
	v_mul_f32_e32 v73, 0x3fb8aa3b, v73
	v_exp_f32_e32 v73, v73
	v_mul_f32_e32 v69, 0.5, v69
	v_cvt_pk_bf16_f32 v68, v72, v68
	v_add_u32_e32 v72, 0xb0, v154
	v_add_f32_e32 v73, 1.0, v73
	v_rcp_f32_e32 v73, v73
	s_nop 0
	v_add_f32_e32 v73, v73, v73
	v_sub_f32_e32 v73, 1.0, v73
	v_add_f32_e32 v73, 1.0, v73
	v_mul_f32_e32 v73, v69, v73
	v_mul_f32_e32 v69, 0x3d372713, v74
	v_mul_f32_e32 v69, v74, v69
	v_fma_f32 v69, v74, v69, v74
	v_mul_f32_e32 v69, 0x3f4c422a, v69
	v_add_f32_e32 v69, v69, v69
	v_mul_f32_e32 v69, 0x3fb8aa3b, v69
	v_exp_f32_e32 v69, v69
	v_mul_f32_e32 v74, 0.5, v74
	v_add_f32_e32 v69, 1.0, v69
	v_rcp_f32_e32 v69, v69
	s_nop 0
	v_add_f32_e32 v69, v69, v69
	v_sub_f32_e32 v69, 1.0, v69
	v_add_f32_e32 v69, 1.0, v69
	v_mul_f32_e32 v69, v74, v69
	v_mul_f32_e32 v74, 0x3d372713, v70
	v_mul_f32_e32 v74, v70, v74
	v_fma_f32 v74, v70, v74, v70
	v_mul_f32_e32 v74, 0x3f4c422a, v74
	v_add_f32_e32 v74, v74, v74
	v_mul_f32_e32 v74, 0x3fb8aa3b, v74
	v_exp_f32_e32 v74, v74
	v_mul_f32_e32 v70, 0.5, v70
	v_add_f32_e32 v74, 1.0, v74
	v_rcp_f32_e32 v74, v74
	s_nop 0
	v_add_f32_e32 v74, v74, v74
	v_sub_f32_e32 v74, 1.0, v74
	v_add_f32_e32 v74, 1.0, v74
	v_mul_f32_e32 v74, v70, v74
	v_mul_f32_e32 v70, 0x3d372713, v75
	v_mul_f32_e32 v70, v75, v70
	v_fma_f32 v70, v75, v70, v75
	v_mul_f32_e32 v70, 0x3f4c422a, v70
	v_add_f32_e32 v70, v70, v70
	v_mul_f32_e32 v70, 0x3fb8aa3b, v70
	v_exp_f32_e32 v70, v70
	v_mul_f32_e32 v75, 0.5, v75
	v_add_f32_e32 v70, 1.0, v70
	v_rcp_f32_e32 v70, v70
	s_nop 0
	v_add_f32_e32 v70, v70, v70
	v_sub_f32_e32 v70, 1.0, v70
	v_add_f32_e32 v70, 1.0, v70
	v_mul_f32_e32 v70, v75, v70
	v_mul_f32_e32 v75, 0x3d372713, v71
	v_mul_f32_e32 v75, v71, v75
	v_fma_f32 v75, v71, v75, v71
	v_mul_f32_e32 v75, 0x3f4c422a, v75
	v_add_f32_e32 v75, v75, v75
	v_mul_f32_e32 v75, 0x3fb8aa3b, v75
	v_exp_f32_e32 v75, v75
	v_cvt_pk_bf16_f32 v69, v69, v70
	v_cvt_pk_bf16_f32 v70, v78, v73
	v_ashrrev_i32_e32 v73, 31, v72
	v_add_f32_e32 v75, 1.0, v75
	v_mul_f32_e32 v71, 0.5, v71
	v_lshlrev_b64 v[72:73], 9, v[72:73]
	v_rcp_f32_e32 v75, v75
	s_nop 0
	v_add_f32_e32 v75, v75, v75
	v_sub_f32_e32 v75, 1.0, v75
	v_add_f32_e32 v75, 1.0, v75
	v_mul_f32_e32 v71, v71, v75
	v_lshl_add_u64 v[78:79], v[146:147], 0, v[72:73]
	v_cvt_pk_bf16_f32 v71, v74, v71
	global_store_dwordx4 v[78:79], v[68:71], off
	global_load_dwordx4 v[68:71], v[152:153], off offset:528
	s_nop 0
	global_load_dwordx4 v[72:75], v[152:153], off offset:512
	s_waitcnt vmcnt(0)
	v_pk_add_f32 v[60:61], v[60:61], v[68:69]
	v_pk_add_f32 v[64:65], v[64:65], v[72:73]
	v_pk_add_f32 v[66:67], v[66:67], v[74:75]
	v_mul_f32_e32 v80, 0x3d372713, v64
	v_mul_f32_e32 v80, v64, v80
	v_fma_f32 v80, v64, v80, v64
	v_mul_f32_e32 v80, 0x3f4c422a, v80
	v_add_f32_e32 v80, v80, v80
	v_mul_f32_e32 v80, 0x3fb8aa3b, v80
	v_exp_f32_e32 v80, v80
	v_mul_f32_e32 v64, 0.5, v64
	v_pk_add_f32 v[62:63], v[62:63], v[70:71]
	v_pk_add_f32 v[56:57], v[56:57], v[72:73]
	v_add_f32_e32 v80, 1.0, v80
	v_pk_add_f32 v[52:53], v[52:53], v[68:69]
	v_pk_add_f32 v[58:59], v[58:59], v[74:75]
	v_pk_add_f32 v[54:55], v[54:55], v[70:71]
	v_rcp_f32_e32 v80, v80
	s_nop 0
	v_add_f32_e32 v80, v80, v80
	v_sub_f32_e32 v80, 1.0, v80
	v_add_f32_e32 v80, 1.0, v80
	v_mul_f32_e32 v64, v64, v80
	v_mul_f32_e32 v80, 0x3d372713, v60
	v_mul_f32_e32 v80, v60, v80
	v_fma_f32 v80, v60, v80, v60
	v_mul_f32_e32 v80, 0x3f4c422a, v80
	v_add_f32_e32 v80, v80, v80
	v_mul_f32_e32 v80, 0x3fb8aa3b, v80
	v_exp_f32_e32 v80, v80
	v_mul_f32_e32 v60, 0.5, v60
	v_pk_add_f32 v[48:49], v[48:49], v[72:73]
	v_pk_add_f32 v[44:45], v[44:45], v[68:69]
	v_add_f32_e32 v80, 1.0, v80
	v_pk_add_f32 v[50:51], v[50:51], v[74:75]
	v_pk_add_f32 v[46:47], v[46:47], v[70:71]
	v_pk_add_f32 v[40:41], v[40:41], v[72:73]
	v_rcp_f32_e32 v80, v80
	s_nop 0
	v_add_f32_e32 v80, v80, v80
	v_sub_f32_e32 v80, 1.0, v80
	v_add_f32_e32 v80, 1.0, v80
	v_mul_f32_e32 v80, v60, v80
	v_mul_f32_e32 v60, 0x3d372713, v65
	v_mul_f32_e32 v60, v65, v60
	v_fma_f32 v60, v65, v60, v65
	v_mul_f32_e32 v60, 0x3f4c422a, v60
	v_add_f32_e32 v60, v60, v60
	v_mul_f32_e32 v60, 0x3fb8aa3b, v60
	v_exp_f32_e32 v60, v60
	v_mul_f32_e32 v65, 0.5, v65
	v_pk_add_f32 v[36:37], v[36:37], v[68:69]
	v_pk_add_f32 v[42:43], v[42:43], v[74:75]
	v_add_f32_e32 v60, 1.0, v60
	v_pk_add_f32 v[38:39], v[38:39], v[70:71]
	v_pk_add_f32 v[32:33], v[32:33], v[72:73]
	v_pk_add_f32 v[28:29], v[28:29], v[68:69]
	v_rcp_f32_e32 v60, v60
	s_nop 0
	v_add_f32_e32 v60, v60, v60
	v_sub_f32_e32 v60, 1.0, v60
	v_add_f32_e32 v60, 1.0, v60
	v_mul_f32_e32 v60, v65, v60
	v_mul_f32_e32 v65, 0x3d372713, v61
	v_mul_f32_e32 v65, v61, v65
	v_fma_f32 v65, v61, v65, v61
	v_mul_f32_e32 v65, 0x3f4c422a, v65
	v_add_f32_e32 v65, v65, v65
	v_mul_f32_e32 v65, 0x3fb8aa3b, v65
	v_exp_f32_e32 v65, v65
	v_mul_f32_e32 v61, 0.5, v61
	v_cvt_pk_bf16_f32 v60, v64, v60
	v_pk_add_f32 v[34:35], v[34:35], v[74:75]
	v_add_f32_e32 v65, 1.0, v65
	v_pk_add_f32 v[30:31], v[30:31], v[70:71]
	v_pk_add_f32 v[24:25], v[24:25], v[72:73]
	v_pk_add_f32 v[20:21], v[20:21], v[68:69]
	v_rcp_f32_e32 v65, v65
	s_nop 0
	v_add_f32_e32 v65, v65, v65
	v_sub_f32_e32 v65, 1.0, v65
	v_add_f32_e32 v65, 1.0, v65
	v_mul_f32_e32 v65, v61, v65
	v_mul_f32_e32 v61, 0x3d372713, v66
	v_mul_f32_e32 v61, v66, v61
	v_fma_f32 v61, v66, v61, v66
	v_mul_f32_e32 v61, 0x3f4c422a, v61
	v_add_f32_e32 v61, v61, v61
	v_mul_f32_e32 v61, 0x3fb8aa3b, v61
	v_exp_f32_e32 v61, v61
	v_mul_f32_e32 v66, 0.5, v66
	v_pk_add_f32 v[26:27], v[26:27], v[74:75]
	v_pk_add_f32 v[22:23], v[22:23], v[70:71]
	v_add_f32_e32 v61, 1.0, v61
	v_pk_add_f32 v[16:17], v[16:17], v[72:73]
	v_pk_add_f32 v[12:13], v[12:13], v[68:69]
	v_pk_add_f32 v[18:19], v[18:19], v[74:75]
	v_rcp_f32_e32 v61, v61
	s_nop 0
	v_add_f32_e32 v61, v61, v61
	v_sub_f32_e32 v61, 1.0, v61
	v_add_f32_e32 v61, 1.0, v61
	v_mul_f32_e32 v61, v66, v61
	v_mul_f32_e32 v66, 0x3d372713, v62
	v_mul_f32_e32 v66, v62, v66
	v_fma_f32 v66, v62, v66, v62
	v_mul_f32_e32 v66, 0x3f4c422a, v66
	v_add_f32_e32 v66, v66, v66
	v_mul_f32_e32 v66, 0x3fb8aa3b, v66
	v_exp_f32_e32 v66, v66
	v_mul_f32_e32 v62, 0.5, v62
	v_pk_add_f32 v[14:15], v[14:15], v[70:71]
	v_pk_add_f32 v[8:9], v[8:9], v[72:73]
	v_add_f32_e32 v66, 1.0, v66
	v_pk_add_f32 v[4:5], v[4:5], v[68:69]
	v_pk_add_f32 v[10:11], v[10:11], v[74:75]
	v_pk_add_f32 v[6:7], v[6:7], v[70:71]
	v_rcp_f32_e32 v66, v66
	s_nop 0
	v_add_f32_e32 v66, v66, v66
	v_sub_f32_e32 v66, 1.0, v66
	v_add_f32_e32 v66, 1.0, v66
	v_mul_f32_e32 v66, v62, v66
	v_mul_f32_e32 v62, 0x3d372713, v67
	v_mul_f32_e32 v62, v67, v62
	v_fma_f32 v62, v67, v62, v67
	v_mul_f32_e32 v62, 0x3f4c422a, v62
	v_add_f32_e32 v62, v62, v62
	v_mul_f32_e32 v62, 0x3fb8aa3b, v62
	v_exp_f32_e32 v62, v62
	v_mul_f32_e32 v67, 0.5, v67
	v_add_f32_e32 v62, 1.0, v62
	v_rcp_f32_e32 v62, v62
	s_nop 0
	v_add_f32_e32 v62, v62, v62
	v_sub_f32_e32 v62, 1.0, v62
	v_add_f32_e32 v62, 1.0, v62
	v_mul_f32_e32 v62, v67, v62
	v_mul_f32_e32 v67, 0x3d372713, v63
	v_mul_f32_e32 v67, v63, v67
	v_fma_f32 v67, v63, v67, v63
	v_mul_f32_e32 v67, 0x3f4c422a, v67
	v_add_f32_e32 v67, v67, v67
	v_mul_f32_e32 v67, 0x3fb8aa3b, v67
	v_exp_f32_e32 v67, v67
	v_mul_f32_e32 v63, 0.5, v63
	v_cvt_pk_bf16_f32 v61, v61, v62
	v_cvt_pk_bf16_f32 v62, v80, v65
	v_add_f32_e32 v67, 1.0, v67
	v_rcp_f32_e32 v67, v67
	s_nop 0
	v_add_f32_e32 v67, v67, v67
	v_sub_f32_e32 v67, 1.0, v67
	v_add_f32_e32 v67, 1.0, v67
	v_mul_f32_e32 v63, v63, v67
	v_cvt_pk_bf16_f32 v63, v66, v63
	global_store_dwordx4 v[132:133], v[60:63], off offset:256
	s_nop 1
	v_mul_f32_e32 v60, 0x3d372713, v56
	v_mul_f32_e32 v60, v56, v60
	v_fma_f32 v60, v56, v60, v56
	v_mul_f32_e32 v60, 0x3f4c422a, v60
	v_add_f32_e32 v60, v60, v60
	v_mul_f32_e32 v60, 0x3fb8aa3b, v60
	v_exp_f32_e32 v60, v60
	v_mul_f32_e32 v56, 0.5, v56
	v_add_f32_e32 v60, 1.0, v60
	v_rcp_f32_e32 v60, v60
	s_nop 0
	v_add_f32_e32 v60, v60, v60
	v_sub_f32_e32 v60, 1.0, v60
	v_add_f32_e32 v60, 1.0, v60
	v_mul_f32_e32 v56, v56, v60
	v_mul_f32_e32 v60, 0x3d372713, v52
	v_mul_f32_e32 v60, v52, v60
	v_fma_f32 v60, v52, v60, v52
	v_mul_f32_e32 v60, 0x3f4c422a, v60
	v_add_f32_e32 v60, v60, v60
	v_mul_f32_e32 v60, 0x3fb8aa3b, v60
	v_exp_f32_e32 v60, v60
	v_mul_f32_e32 v52, 0.5, v52
	v_add_f32_e32 v60, 1.0, v60
	v_rcp_f32_e32 v60, v60
	s_nop 0
	v_add_f32_e32 v60, v60, v60
	v_sub_f32_e32 v60, 1.0, v60
	v_add_f32_e32 v60, 1.0, v60
	v_mul_f32_e32 v60, v52, v60
	v_mul_f32_e32 v52, 0x3d372713, v57
	v_mul_f32_e32 v52, v57, v52
	v_fma_f32 v52, v57, v52, v57
	v_mul_f32_e32 v52, 0x3f4c422a, v52
	v_add_f32_e32 v52, v52, v52
	v_mul_f32_e32 v52, 0x3fb8aa3b, v52
	v_exp_f32_e32 v52, v52
	v_mul_f32_e32 v57, 0.5, v57
	v_add_f32_e32 v52, 1.0, v52
	v_rcp_f32_e32 v52, v52
	s_nop 0
	v_add_f32_e32 v52, v52, v52
	v_sub_f32_e32 v52, 1.0, v52
	v_add_f32_e32 v52, 1.0, v52
	v_mul_f32_e32 v52, v57, v52
	v_mul_f32_e32 v57, 0x3d372713, v53
	v_mul_f32_e32 v57, v53, v57
	v_fma_f32 v57, v53, v57, v53
	v_mul_f32_e32 v57, 0x3f4c422a, v57
	v_add_f32_e32 v57, v57, v57
	v_mul_f32_e32 v57, 0x3fb8aa3b, v57
	v_exp_f32_e32 v57, v57
	v_mul_f32_e32 v53, 0.5, v53
	v_cvt_pk_bf16_f32 v52, v56, v52
	v_add_f32_e32 v57, 1.0, v57
	v_rcp_f32_e32 v57, v57
	s_nop 0
	v_add_f32_e32 v57, v57, v57
	v_sub_f32_e32 v57, 1.0, v57
	v_add_f32_e32 v57, 1.0, v57
	v_mul_f32_e32 v57, v53, v57
	v_mul_f32_e32 v53, 0x3d372713, v58
	v_mul_f32_e32 v53, v58, v53
	v_fma_f32 v53, v58, v53, v58
	v_mul_f32_e32 v53, 0x3f4c422a, v53
	v_add_f32_e32 v53, v53, v53
	v_mul_f32_e32 v53, 0x3fb8aa3b, v53
	v_exp_f32_e32 v53, v53
	v_mul_f32_e32 v58, 0.5, v58
	v_add_f32_e32 v53, 1.0, v53
	v_rcp_f32_e32 v53, v53
	s_nop 0
	v_add_f32_e32 v53, v53, v53
	v_sub_f32_e32 v53, 1.0, v53
	v_add_f32_e32 v53, 1.0, v53
	v_mul_f32_e32 v53, v58, v53
	v_mul_f32_e32 v58, 0x3d372713, v54
	v_mul_f32_e32 v58, v54, v58
	v_fma_f32 v58, v54, v58, v54
	v_mul_f32_e32 v58, 0x3f4c422a, v58
	v_add_f32_e32 v58, v58, v58
	v_mul_f32_e32 v58, 0x3fb8aa3b, v58
	v_exp_f32_e32 v58, v58
	v_mul_f32_e32 v54, 0.5, v54
	v_add_f32_e32 v58, 1.0, v58
	v_rcp_f32_e32 v58, v58
	s_nop 0
	v_add_f32_e32 v58, v58, v58
	v_sub_f32_e32 v58, 1.0, v58
	v_add_f32_e32 v58, 1.0, v58
	v_mul_f32_e32 v58, v54, v58
	v_mul_f32_e32 v54, 0x3d372713, v59
	v_mul_f32_e32 v54, v59, v54
	v_fma_f32 v54, v59, v54, v59
	v_mul_f32_e32 v54, 0x3f4c422a, v54
	v_add_f32_e32 v54, v54, v54
	v_mul_f32_e32 v54, 0x3fb8aa3b, v54
	v_exp_f32_e32 v54, v54
	v_mul_f32_e32 v59, 0.5, v59
	v_add_f32_e32 v54, 1.0, v54
	v_rcp_f32_e32 v54, v54
	s_nop 0
	v_add_f32_e32 v54, v54, v54
	v_sub_f32_e32 v54, 1.0, v54
	v_add_f32_e32 v54, 1.0, v54
	v_mul_f32_e32 v54, v59, v54
	v_mul_f32_e32 v59, 0x3d372713, v55
	v_mul_f32_e32 v59, v55, v59
	v_fma_f32 v59, v55, v59, v55
	v_mul_f32_e32 v59, 0x3f4c422a, v59
	v_add_f32_e32 v59, v59, v59
	v_mul_f32_e32 v59, 0x3fb8aa3b, v59
	v_exp_f32_e32 v59, v59
	v_mul_f32_e32 v55, 0.5, v55
	v_cvt_pk_bf16_f32 v53, v53, v54
	v_cvt_pk_bf16_f32 v54, v60, v57
	v_add_f32_e32 v59, 1.0, v59
	v_rcp_f32_e32 v59, v59
	s_nop 0
	v_add_f32_e32 v59, v59, v59
	v_sub_f32_e32 v59, 1.0, v59
	v_add_f32_e32 v59, 1.0, v59
	v_mul_f32_e32 v55, v55, v59
	v_cvt_pk_bf16_f32 v55, v58, v55
	global_store_dwordx4 v[124:125], v[52:55], off offset:256
	s_nop 1
	v_mul_f32_e32 v52, 0x3d372713, v48
	v_mul_f32_e32 v52, v48, v52
	v_fma_f32 v52, v48, v52, v48
	v_mul_f32_e32 v52, 0x3f4c422a, v52
	v_add_f32_e32 v52, v52, v52
	v_mul_f32_e32 v52, 0x3fb8aa3b, v52
	v_exp_f32_e32 v52, v52
	v_mul_f32_e32 v48, 0.5, v48
	v_add_f32_e32 v52, 1.0, v52
	v_rcp_f32_e32 v52, v52
	s_nop 0
	v_add_f32_e32 v52, v52, v52
	v_sub_f32_e32 v52, 1.0, v52
	v_add_f32_e32 v52, 1.0, v52
	v_mul_f32_e32 v48, v48, v52
	v_mul_f32_e32 v52, 0x3d372713, v44
	v_mul_f32_e32 v52, v44, v52
	v_fma_f32 v52, v44, v52, v44
	v_mul_f32_e32 v52, 0x3f4c422a, v52
	v_add_f32_e32 v52, v52, v52
	v_mul_f32_e32 v52, 0x3fb8aa3b, v52
	v_exp_f32_e32 v52, v52
	v_mul_f32_e32 v44, 0.5, v44
	v_add_f32_e32 v52, 1.0, v52
	v_rcp_f32_e32 v52, v52
	s_nop 0
	v_add_f32_e32 v52, v52, v52
	v_sub_f32_e32 v52, 1.0, v52
	v_add_f32_e32 v52, 1.0, v52
	v_mul_f32_e32 v52, v44, v52
	v_mul_f32_e32 v44, 0x3d372713, v49
	v_mul_f32_e32 v44, v49, v44
	v_fma_f32 v44, v49, v44, v49
	v_mul_f32_e32 v44, 0x3f4c422a, v44
	v_add_f32_e32 v44, v44, v44
	v_mul_f32_e32 v44, 0x3fb8aa3b, v44
	v_exp_f32_e32 v44, v44
	v_mul_f32_e32 v49, 0.5, v49
	v_add_f32_e32 v44, 1.0, v44
	v_rcp_f32_e32 v44, v44
	s_nop 0
	v_add_f32_e32 v44, v44, v44
	v_sub_f32_e32 v44, 1.0, v44
	v_add_f32_e32 v44, 1.0, v44
	v_mul_f32_e32 v44, v49, v44
	v_mul_f32_e32 v49, 0x3d372713, v45
	v_mul_f32_e32 v49, v45, v49
	v_fma_f32 v49, v45, v49, v45
	v_mul_f32_e32 v49, 0x3f4c422a, v49
	v_add_f32_e32 v49, v49, v49
	v_mul_f32_e32 v49, 0x3fb8aa3b, v49
	v_exp_f32_e32 v49, v49
	v_mul_f32_e32 v45, 0.5, v45
	v_cvt_pk_bf16_f32 v44, v48, v44
	v_add_f32_e32 v49, 1.0, v49
	v_rcp_f32_e32 v49, v49
	s_nop 0
	v_add_f32_e32 v49, v49, v49
	v_sub_f32_e32 v49, 1.0, v49
	v_add_f32_e32 v49, 1.0, v49
	v_mul_f32_e32 v49, v45, v49
	v_mul_f32_e32 v45, 0x3d372713, v50
	v_mul_f32_e32 v45, v50, v45
	v_fma_f32 v45, v50, v45, v50
	v_mul_f32_e32 v45, 0x3f4c422a, v45
	v_add_f32_e32 v45, v45, v45
	v_mul_f32_e32 v45, 0x3fb8aa3b, v45
	v_exp_f32_e32 v45, v45
	v_mul_f32_e32 v50, 0.5, v50
	v_add_f32_e32 v45, 1.0, v45
	v_rcp_f32_e32 v45, v45
	s_nop 0
	v_add_f32_e32 v45, v45, v45
	v_sub_f32_e32 v45, 1.0, v45
	v_add_f32_e32 v45, 1.0, v45
	v_mul_f32_e32 v45, v50, v45
	v_mul_f32_e32 v50, 0x3d372713, v46
	v_mul_f32_e32 v50, v46, v50
	v_fma_f32 v50, v46, v50, v46
	v_mul_f32_e32 v50, 0x3f4c422a, v50
	v_add_f32_e32 v50, v50, v50
	v_mul_f32_e32 v50, 0x3fb8aa3b, v50
	v_exp_f32_e32 v50, v50
	v_mul_f32_e32 v46, 0.5, v46
	v_add_f32_e32 v50, 1.0, v50
	v_rcp_f32_e32 v50, v50
	s_nop 0
	v_add_f32_e32 v50, v50, v50
	v_sub_f32_e32 v50, 1.0, v50
	v_add_f32_e32 v50, 1.0, v50
	v_mul_f32_e32 v50, v46, v50
	v_mul_f32_e32 v46, 0x3d372713, v51
	v_mul_f32_e32 v46, v51, v46
	v_fma_f32 v46, v51, v46, v51
	v_mul_f32_e32 v46, 0x3f4c422a, v46
	v_add_f32_e32 v46, v46, v46
	v_mul_f32_e32 v46, 0x3fb8aa3b, v46
	v_exp_f32_e32 v46, v46
	v_mul_f32_e32 v51, 0.5, v51
	v_add_f32_e32 v46, 1.0, v46
	v_rcp_f32_e32 v46, v46
	s_nop 0
	v_add_f32_e32 v46, v46, v46
	v_sub_f32_e32 v46, 1.0, v46
	v_add_f32_e32 v46, 1.0, v46
	v_mul_f32_e32 v46, v51, v46
	v_mul_f32_e32 v51, 0x3d372713, v47
	v_mul_f32_e32 v51, v47, v51
	v_fma_f32 v51, v47, v51, v47
	v_mul_f32_e32 v51, 0x3f4c422a, v51
	v_add_f32_e32 v51, v51, v51
	v_mul_f32_e32 v51, 0x3fb8aa3b, v51
	v_exp_f32_e32 v51, v51
	v_mul_f32_e32 v47, 0.5, v47
	v_cvt_pk_bf16_f32 v45, v45, v46
	v_cvt_pk_bf16_f32 v46, v52, v49
	v_add_f32_e32 v51, 1.0, v51
	v_rcp_f32_e32 v51, v51
	s_nop 0
	v_add_f32_e32 v51, v51, v51
	v_sub_f32_e32 v51, 1.0, v51
	v_add_f32_e32 v51, 1.0, v51
	v_mul_f32_e32 v47, v47, v51
	v_cvt_pk_bf16_f32 v47, v50, v47
	global_store_dwordx4 v[116:117], v[44:47], off offset:256
	s_nop 1
	v_mul_f32_e32 v44, 0x3d372713, v40
	v_mul_f32_e32 v44, v40, v44
	v_fma_f32 v44, v40, v44, v40
	v_mul_f32_e32 v44, 0x3f4c422a, v44
	v_add_f32_e32 v44, v44, v44
	v_mul_f32_e32 v44, 0x3fb8aa3b, v44
	v_exp_f32_e32 v44, v44
	v_mul_f32_e32 v40, 0.5, v40
	v_add_f32_e32 v44, 1.0, v44
	v_rcp_f32_e32 v44, v44
	s_nop 0
	v_add_f32_e32 v44, v44, v44
	v_sub_f32_e32 v44, 1.0, v44
	v_add_f32_e32 v44, 1.0, v44
	v_mul_f32_e32 v40, v40, v44
	v_mul_f32_e32 v44, 0x3d372713, v36
	v_mul_f32_e32 v44, v36, v44
	v_fma_f32 v44, v36, v44, v36
	v_mul_f32_e32 v44, 0x3f4c422a, v44
	v_add_f32_e32 v44, v44, v44
	v_mul_f32_e32 v44, 0x3fb8aa3b, v44
	v_exp_f32_e32 v44, v44
	v_mul_f32_e32 v36, 0.5, v36
	v_add_f32_e32 v44, 1.0, v44
	v_rcp_f32_e32 v44, v44
	s_nop 0
	v_add_f32_e32 v44, v44, v44
	v_sub_f32_e32 v44, 1.0, v44
	v_add_f32_e32 v44, 1.0, v44
	v_mul_f32_e32 v44, v36, v44
	v_mul_f32_e32 v36, 0x3d372713, v41
	v_mul_f32_e32 v36, v41, v36
	v_fma_f32 v36, v41, v36, v41
	v_mul_f32_e32 v36, 0x3f4c422a, v36
	v_add_f32_e32 v36, v36, v36
	v_mul_f32_e32 v36, 0x3fb8aa3b, v36
	v_exp_f32_e32 v36, v36
	v_mul_f32_e32 v41, 0.5, v41
	v_add_f32_e32 v36, 1.0, v36
	v_rcp_f32_e32 v36, v36
	s_nop 0
	v_add_f32_e32 v36, v36, v36
	v_sub_f32_e32 v36, 1.0, v36
	v_add_f32_e32 v36, 1.0, v36
	v_mul_f32_e32 v36, v41, v36
	v_mul_f32_e32 v41, 0x3d372713, v37
	v_mul_f32_e32 v41, v37, v41
	v_fma_f32 v41, v37, v41, v37
	v_mul_f32_e32 v41, 0x3f4c422a, v41
	v_add_f32_e32 v41, v41, v41
	v_mul_f32_e32 v41, 0x3fb8aa3b, v41
	v_exp_f32_e32 v41, v41
	v_mul_f32_e32 v37, 0.5, v37
	v_cvt_pk_bf16_f32 v36, v40, v36
	v_add_f32_e32 v41, 1.0, v41
	v_rcp_f32_e32 v41, v41
	s_nop 0
	v_add_f32_e32 v41, v41, v41
	v_sub_f32_e32 v41, 1.0, v41
	v_add_f32_e32 v41, 1.0, v41
	v_mul_f32_e32 v41, v37, v41
	v_mul_f32_e32 v37, 0x3d372713, v42
	v_mul_f32_e32 v37, v42, v37
	v_fma_f32 v37, v42, v37, v42
	v_mul_f32_e32 v37, 0x3f4c422a, v37
	v_add_f32_e32 v37, v37, v37
	v_mul_f32_e32 v37, 0x3fb8aa3b, v37
	v_exp_f32_e32 v37, v37
	v_mul_f32_e32 v42, 0.5, v42
	v_add_f32_e32 v37, 1.0, v37
	v_rcp_f32_e32 v37, v37
	s_nop 0
	v_add_f32_e32 v37, v37, v37
	v_sub_f32_e32 v37, 1.0, v37
	v_add_f32_e32 v37, 1.0, v37
	v_mul_f32_e32 v37, v42, v37
	v_mul_f32_e32 v42, 0x3d372713, v38
	v_mul_f32_e32 v42, v38, v42
	v_fma_f32 v42, v38, v42, v38
	v_mul_f32_e32 v42, 0x3f4c422a, v42
	v_add_f32_e32 v42, v42, v42
	v_mul_f32_e32 v42, 0x3fb8aa3b, v42
	v_exp_f32_e32 v42, v42
	v_mul_f32_e32 v38, 0.5, v38
	v_add_f32_e32 v42, 1.0, v42
	v_rcp_f32_e32 v42, v42
	s_nop 0
	v_add_f32_e32 v42, v42, v42
	v_sub_f32_e32 v42, 1.0, v42
	v_add_f32_e32 v42, 1.0, v42
	v_mul_f32_e32 v42, v38, v42
	v_mul_f32_e32 v38, 0x3d372713, v43
	v_mul_f32_e32 v38, v43, v38
	v_fma_f32 v38, v43, v38, v43
	v_mul_f32_e32 v38, 0x3f4c422a, v38
	v_add_f32_e32 v38, v38, v38
	v_mul_f32_e32 v38, 0x3fb8aa3b, v38
	v_exp_f32_e32 v38, v38
	v_mul_f32_e32 v43, 0.5, v43
	v_add_f32_e32 v38, 1.0, v38
	v_rcp_f32_e32 v38, v38
	s_nop 0
	v_add_f32_e32 v38, v38, v38
	v_sub_f32_e32 v38, 1.0, v38
	v_add_f32_e32 v38, 1.0, v38
	v_mul_f32_e32 v38, v43, v38
	v_mul_f32_e32 v43, 0x3d372713, v39
	v_mul_f32_e32 v43, v39, v43
	v_fma_f32 v43, v39, v43, v39
	v_mul_f32_e32 v43, 0x3f4c422a, v43
	v_add_f32_e32 v43, v43, v43
	v_mul_f32_e32 v43, 0x3fb8aa3b, v43
	v_exp_f32_e32 v43, v43
	v_mul_f32_e32 v39, 0.5, v39
	v_cvt_pk_bf16_f32 v37, v37, v38
	v_cvt_pk_bf16_f32 v38, v44, v41
	v_add_f32_e32 v43, 1.0, v43
	v_rcp_f32_e32 v43, v43
	s_nop 0
	v_add_f32_e32 v43, v43, v43
	v_sub_f32_e32 v43, 1.0, v43
	v_add_f32_e32 v43, 1.0, v43
	v_mul_f32_e32 v39, v39, v43
	v_cvt_pk_bf16_f32 v39, v42, v39
	global_store_dwordx4 v[108:109], v[36:39], off offset:256
	s_nop 1
	v_mul_f32_e32 v36, 0x3d372713, v32
	v_mul_f32_e32 v36, v32, v36
	v_fma_f32 v36, v32, v36, v32
	v_mul_f32_e32 v36, 0x3f4c422a, v36
	v_add_f32_e32 v36, v36, v36
	v_mul_f32_e32 v36, 0x3fb8aa3b, v36
	v_exp_f32_e32 v36, v36
	v_mul_f32_e32 v32, 0.5, v32
	v_add_f32_e32 v36, 1.0, v36
	v_rcp_f32_e32 v36, v36
	s_nop 0
	v_add_f32_e32 v36, v36, v36
	v_sub_f32_e32 v36, 1.0, v36
	v_add_f32_e32 v36, 1.0, v36
	v_mul_f32_e32 v32, v32, v36
	v_mul_f32_e32 v36, 0x3d372713, v28
	v_mul_f32_e32 v36, v28, v36
	v_fma_f32 v36, v28, v36, v28
	v_mul_f32_e32 v36, 0x3f4c422a, v36
	v_add_f32_e32 v36, v36, v36
	v_mul_f32_e32 v36, 0x3fb8aa3b, v36
	v_exp_f32_e32 v36, v36
	v_mul_f32_e32 v28, 0.5, v28
	v_add_f32_e32 v36, 1.0, v36
	v_rcp_f32_e32 v36, v36
	s_nop 0
	v_add_f32_e32 v36, v36, v36
	v_sub_f32_e32 v36, 1.0, v36
	v_add_f32_e32 v36, 1.0, v36
	v_mul_f32_e32 v36, v28, v36
	v_mul_f32_e32 v28, 0x3d372713, v33
	v_mul_f32_e32 v28, v33, v28
	v_fma_f32 v28, v33, v28, v33
	v_mul_f32_e32 v28, 0x3f4c422a, v28
	v_add_f32_e32 v28, v28, v28
	v_mul_f32_e32 v28, 0x3fb8aa3b, v28
	v_exp_f32_e32 v28, v28
	v_mul_f32_e32 v33, 0.5, v33
	v_add_f32_e32 v28, 1.0, v28
	v_rcp_f32_e32 v28, v28
	s_nop 0
	v_add_f32_e32 v28, v28, v28
	v_sub_f32_e32 v28, 1.0, v28
	v_add_f32_e32 v28, 1.0, v28
	v_mul_f32_e32 v28, v33, v28
	v_mul_f32_e32 v33, 0x3d372713, v29
	v_mul_f32_e32 v33, v29, v33
	v_fma_f32 v33, v29, v33, v29
	v_mul_f32_e32 v33, 0x3f4c422a, v33
	v_add_f32_e32 v33, v33, v33
	v_mul_f32_e32 v33, 0x3fb8aa3b, v33
	v_exp_f32_e32 v33, v33
	v_mul_f32_e32 v29, 0.5, v29
	v_cvt_pk_bf16_f32 v28, v32, v28
	v_add_f32_e32 v33, 1.0, v33
	v_rcp_f32_e32 v33, v33
	s_nop 0
	v_add_f32_e32 v33, v33, v33
	v_sub_f32_e32 v33, 1.0, v33
	v_add_f32_e32 v33, 1.0, v33
	v_mul_f32_e32 v33, v29, v33
	v_mul_f32_e32 v29, 0x3d372713, v34
	v_mul_f32_e32 v29, v34, v29
	v_fma_f32 v29, v34, v29, v34
	v_mul_f32_e32 v29, 0x3f4c422a, v29
	v_add_f32_e32 v29, v29, v29
	v_mul_f32_e32 v29, 0x3fb8aa3b, v29
	v_exp_f32_e32 v29, v29
	v_mul_f32_e32 v34, 0.5, v34
	v_add_f32_e32 v29, 1.0, v29
	v_rcp_f32_e32 v29, v29
	s_nop 0
	v_add_f32_e32 v29, v29, v29
	v_sub_f32_e32 v29, 1.0, v29
	v_add_f32_e32 v29, 1.0, v29
	v_mul_f32_e32 v29, v34, v29
	v_mul_f32_e32 v34, 0x3d372713, v30
	v_mul_f32_e32 v34, v30, v34
	v_fma_f32 v34, v30, v34, v30
	v_mul_f32_e32 v34, 0x3f4c422a, v34
	v_add_f32_e32 v34, v34, v34
	v_mul_f32_e32 v34, 0x3fb8aa3b, v34
	v_exp_f32_e32 v34, v34
	v_mul_f32_e32 v30, 0.5, v30
	v_add_f32_e32 v34, 1.0, v34
	v_rcp_f32_e32 v34, v34
	s_nop 0
	v_add_f32_e32 v34, v34, v34
	v_sub_f32_e32 v34, 1.0, v34
	v_add_f32_e32 v34, 1.0, v34
	v_mul_f32_e32 v34, v30, v34
	v_mul_f32_e32 v30, 0x3d372713, v35
	v_mul_f32_e32 v30, v35, v30
	v_fma_f32 v30, v35, v30, v35
	v_mul_f32_e32 v30, 0x3f4c422a, v30
	v_add_f32_e32 v30, v30, v30
	v_mul_f32_e32 v30, 0x3fb8aa3b, v30
	v_exp_f32_e32 v30, v30
	v_mul_f32_e32 v35, 0.5, v35
	v_add_f32_e32 v30, 1.0, v30
	v_rcp_f32_e32 v30, v30
	s_nop 0
	v_add_f32_e32 v30, v30, v30
	v_sub_f32_e32 v30, 1.0, v30
	v_add_f32_e32 v30, 1.0, v30
	v_mul_f32_e32 v30, v35, v30
	v_mul_f32_e32 v35, 0x3d372713, v31
	v_mul_f32_e32 v35, v31, v35
	v_fma_f32 v35, v31, v35, v31
	v_mul_f32_e32 v35, 0x3f4c422a, v35
	v_add_f32_e32 v35, v35, v35
	v_mul_f32_e32 v35, 0x3fb8aa3b, v35
	v_exp_f32_e32 v35, v35
	v_mul_f32_e32 v31, 0.5, v31
	v_cvt_pk_bf16_f32 v29, v29, v30
	v_cvt_pk_bf16_f32 v30, v36, v33
	v_add_f32_e32 v35, 1.0, v35
	v_rcp_f32_e32 v35, v35
	s_nop 0
	v_add_f32_e32 v35, v35, v35
	v_sub_f32_e32 v35, 1.0, v35
	v_add_f32_e32 v35, 1.0, v35
	v_mul_f32_e32 v31, v31, v35
	v_cvt_pk_bf16_f32 v31, v34, v31
	global_store_dwordx4 v[100:101], v[28:31], off offset:256
	s_nop 1
	v_mul_f32_e32 v28, 0x3d372713, v24
	v_mul_f32_e32 v28, v24, v28
	v_fma_f32 v28, v24, v28, v24
	v_mul_f32_e32 v28, 0x3f4c422a, v28
	v_add_f32_e32 v28, v28, v28
	v_mul_f32_e32 v28, 0x3fb8aa3b, v28
	v_exp_f32_e32 v28, v28
	v_mul_f32_e32 v24, 0.5, v24
	v_add_f32_e32 v28, 1.0, v28
	v_rcp_f32_e32 v28, v28
	s_nop 0
	v_add_f32_e32 v28, v28, v28
	v_sub_f32_e32 v28, 1.0, v28
	v_add_f32_e32 v28, 1.0, v28
	v_mul_f32_e32 v24, v24, v28
	v_mul_f32_e32 v28, 0x3d372713, v20
	v_mul_f32_e32 v28, v20, v28
	v_fma_f32 v28, v20, v28, v20
	v_mul_f32_e32 v28, 0x3f4c422a, v28
	v_add_f32_e32 v28, v28, v28
	v_mul_f32_e32 v28, 0x3fb8aa3b, v28
	v_exp_f32_e32 v28, v28
	v_mul_f32_e32 v20, 0.5, v20
	v_add_f32_e32 v28, 1.0, v28
	v_rcp_f32_e32 v28, v28
	s_nop 0
	v_add_f32_e32 v28, v28, v28
	v_sub_f32_e32 v28, 1.0, v28
	v_add_f32_e32 v28, 1.0, v28
	v_mul_f32_e32 v28, v20, v28
	v_mul_f32_e32 v20, 0x3d372713, v25
	v_mul_f32_e32 v20, v25, v20
	v_fma_f32 v20, v25, v20, v25
	v_mul_f32_e32 v20, 0x3f4c422a, v20
	v_add_f32_e32 v20, v20, v20
	v_mul_f32_e32 v20, 0x3fb8aa3b, v20
	v_exp_f32_e32 v20, v20
	v_mul_f32_e32 v25, 0.5, v25
	v_add_f32_e32 v20, 1.0, v20
	v_rcp_f32_e32 v20, v20
	s_nop 0
	v_add_f32_e32 v20, v20, v20
	v_sub_f32_e32 v20, 1.0, v20
	v_add_f32_e32 v20, 1.0, v20
	v_mul_f32_e32 v20, v25, v20
	v_mul_f32_e32 v25, 0x3d372713, v21
	v_mul_f32_e32 v25, v21, v25
	v_fma_f32 v25, v21, v25, v21
	v_mul_f32_e32 v25, 0x3f4c422a, v25
	v_add_f32_e32 v25, v25, v25
	v_mul_f32_e32 v25, 0x3fb8aa3b, v25
	v_exp_f32_e32 v25, v25
	v_mul_f32_e32 v21, 0.5, v21
	v_cvt_pk_bf16_f32 v20, v24, v20
	v_add_f32_e32 v25, 1.0, v25
	v_rcp_f32_e32 v25, v25
	s_nop 0
	v_add_f32_e32 v25, v25, v25
	v_sub_f32_e32 v25, 1.0, v25
	v_add_f32_e32 v25, 1.0, v25
	v_mul_f32_e32 v25, v21, v25
	v_mul_f32_e32 v21, 0x3d372713, v26
	v_mul_f32_e32 v21, v26, v21
	v_fma_f32 v21, v26, v21, v26
	v_mul_f32_e32 v21, 0x3f4c422a, v21
	v_add_f32_e32 v21, v21, v21
	v_mul_f32_e32 v21, 0x3fb8aa3b, v21
	v_exp_f32_e32 v21, v21
	v_mul_f32_e32 v26, 0.5, v26
	v_add_f32_e32 v21, 1.0, v21
	v_rcp_f32_e32 v21, v21
	s_nop 0
	v_add_f32_e32 v21, v21, v21
	v_sub_f32_e32 v21, 1.0, v21
	v_add_f32_e32 v21, 1.0, v21
	v_mul_f32_e32 v21, v26, v21
	v_mul_f32_e32 v26, 0x3d372713, v22
	v_mul_f32_e32 v26, v22, v26
	v_fma_f32 v26, v22, v26, v22
	v_mul_f32_e32 v26, 0x3f4c422a, v26
	v_add_f32_e32 v26, v26, v26
	v_mul_f32_e32 v26, 0x3fb8aa3b, v26
	v_exp_f32_e32 v26, v26
	v_mul_f32_e32 v22, 0.5, v22
	v_add_f32_e32 v26, 1.0, v26
	v_rcp_f32_e32 v26, v26
	s_nop 0
	v_add_f32_e32 v26, v26, v26
	v_sub_f32_e32 v26, 1.0, v26
	v_add_f32_e32 v26, 1.0, v26
	v_mul_f32_e32 v26, v22, v26
	v_mul_f32_e32 v22, 0x3d372713, v27
	v_mul_f32_e32 v22, v27, v22
	v_fma_f32 v22, v27, v22, v27
	v_mul_f32_e32 v22, 0x3f4c422a, v22
	v_add_f32_e32 v22, v22, v22
	v_mul_f32_e32 v22, 0x3fb8aa3b, v22
	v_exp_f32_e32 v22, v22
	v_mul_f32_e32 v27, 0.5, v27
	v_add_f32_e32 v22, 1.0, v22
	v_rcp_f32_e32 v22, v22
	s_nop 0
	v_add_f32_e32 v22, v22, v22
	v_sub_f32_e32 v22, 1.0, v22
	v_add_f32_e32 v22, 1.0, v22
	v_mul_f32_e32 v22, v27, v22
	v_mul_f32_e32 v27, 0x3d372713, v23
	v_mul_f32_e32 v27, v23, v27
	v_fma_f32 v27, v23, v27, v23
	v_mul_f32_e32 v27, 0x3f4c422a, v27
	v_add_f32_e32 v27, v27, v27
	v_mul_f32_e32 v27, 0x3fb8aa3b, v27
	v_exp_f32_e32 v27, v27
	v_mul_f32_e32 v23, 0.5, v23
	v_cvt_pk_bf16_f32 v21, v21, v22
	v_cvt_pk_bf16_f32 v22, v28, v25
	v_add_f32_e32 v27, 1.0, v27
	v_rcp_f32_e32 v27, v27
	s_nop 0
	v_add_f32_e32 v27, v27, v27
	v_sub_f32_e32 v27, 1.0, v27
	v_add_f32_e32 v27, 1.0, v27
	v_mul_f32_e32 v23, v23, v27
	v_cvt_pk_bf16_f32 v23, v26, v23
	global_store_dwordx4 v[92:93], v[20:23], off offset:256
	s_nop 1
	v_mul_f32_e32 v20, 0x3d372713, v16
	v_mul_f32_e32 v20, v16, v20
	v_fma_f32 v20, v16, v20, v16
	v_mul_f32_e32 v20, 0x3f4c422a, v20
	v_add_f32_e32 v20, v20, v20
	v_mul_f32_e32 v20, 0x3fb8aa3b, v20
	v_exp_f32_e32 v20, v20
	v_mul_f32_e32 v16, 0.5, v16
	v_add_f32_e32 v20, 1.0, v20
	v_rcp_f32_e32 v20, v20
	s_nop 0
	v_add_f32_e32 v20, v20, v20
	v_sub_f32_e32 v20, 1.0, v20
	v_add_f32_e32 v20, 1.0, v20
	v_mul_f32_e32 v16, v16, v20
	v_mul_f32_e32 v20, 0x3d372713, v12
	v_mul_f32_e32 v20, v12, v20
	v_fma_f32 v20, v12, v20, v12
	v_mul_f32_e32 v20, 0x3f4c422a, v20
	v_add_f32_e32 v20, v20, v20
	v_mul_f32_e32 v20, 0x3fb8aa3b, v20
	v_exp_f32_e32 v20, v20
	v_mul_f32_e32 v12, 0.5, v12
	v_add_f32_e32 v20, 1.0, v20
	v_rcp_f32_e32 v20, v20
	s_nop 0
	v_add_f32_e32 v20, v20, v20
	v_sub_f32_e32 v20, 1.0, v20
	v_add_f32_e32 v20, 1.0, v20
	v_mul_f32_e32 v20, v12, v20
	v_mul_f32_e32 v12, 0x3d372713, v17
	v_mul_f32_e32 v12, v17, v12
	v_fma_f32 v12, v17, v12, v17
	v_mul_f32_e32 v12, 0x3f4c422a, v12
	v_add_f32_e32 v12, v12, v12
	v_mul_f32_e32 v12, 0x3fb8aa3b, v12
	v_exp_f32_e32 v12, v12
	v_mul_f32_e32 v17, 0.5, v17
	v_add_f32_e32 v12, 1.0, v12
	v_rcp_f32_e32 v12, v12
	s_nop 0
	v_add_f32_e32 v12, v12, v12
	v_sub_f32_e32 v12, 1.0, v12
	v_add_f32_e32 v12, 1.0, v12
	v_mul_f32_e32 v12, v17, v12
	v_mul_f32_e32 v17, 0x3d372713, v13
	v_mul_f32_e32 v17, v13, v17
	v_fma_f32 v17, v13, v17, v13
	v_mul_f32_e32 v17, 0x3f4c422a, v17
	v_add_f32_e32 v17, v17, v17
	v_mul_f32_e32 v17, 0x3fb8aa3b, v17
	v_exp_f32_e32 v17, v17
	v_mul_f32_e32 v13, 0.5, v13
	v_cvt_pk_bf16_f32 v12, v16, v12
	v_add_f32_e32 v17, 1.0, v17
	v_rcp_f32_e32 v17, v17
	s_nop 0
	v_add_f32_e32 v17, v17, v17
	v_sub_f32_e32 v17, 1.0, v17
	v_add_f32_e32 v17, 1.0, v17
	v_mul_f32_e32 v17, v13, v17
	v_mul_f32_e32 v13, 0x3d372713, v18
	v_mul_f32_e32 v13, v18, v13
	v_fma_f32 v13, v18, v13, v18
	v_mul_f32_e32 v13, 0x3f4c422a, v13
	v_add_f32_e32 v13, v13, v13
	v_mul_f32_e32 v13, 0x3fb8aa3b, v13
	v_exp_f32_e32 v13, v13
	v_mul_f32_e32 v18, 0.5, v18
	v_add_f32_e32 v13, 1.0, v13
	v_rcp_f32_e32 v13, v13
	s_nop 0
	v_add_f32_e32 v13, v13, v13
	v_sub_f32_e32 v13, 1.0, v13
	v_add_f32_e32 v13, 1.0, v13
	v_mul_f32_e32 v13, v18, v13
	v_mul_f32_e32 v18, 0x3d372713, v14
	v_mul_f32_e32 v18, v14, v18
	v_fma_f32 v18, v14, v18, v14
	v_mul_f32_e32 v18, 0x3f4c422a, v18
	v_add_f32_e32 v18, v18, v18
	v_mul_f32_e32 v18, 0x3fb8aa3b, v18
	v_exp_f32_e32 v18, v18
	v_mul_f32_e32 v14, 0.5, v14
	v_add_f32_e32 v18, 1.0, v18
	v_rcp_f32_e32 v18, v18
	s_nop 0
	v_add_f32_e32 v18, v18, v18
	v_sub_f32_e32 v18, 1.0, v18
	v_add_f32_e32 v18, 1.0, v18
	v_mul_f32_e32 v18, v14, v18
	v_mul_f32_e32 v14, 0x3d372713, v19
	v_mul_f32_e32 v14, v19, v14
	v_fma_f32 v14, v19, v14, v19
	v_mul_f32_e32 v14, 0x3f4c422a, v14
	v_add_f32_e32 v14, v14, v14
	v_mul_f32_e32 v14, 0x3fb8aa3b, v14
	v_exp_f32_e32 v14, v14
	v_mul_f32_e32 v19, 0.5, v19
	v_add_f32_e32 v14, 1.0, v14
	v_rcp_f32_e32 v14, v14
	s_nop 0
	v_add_f32_e32 v14, v14, v14
	v_sub_f32_e32 v14, 1.0, v14
	v_add_f32_e32 v14, 1.0, v14
	v_mul_f32_e32 v14, v19, v14
	v_mul_f32_e32 v19, 0x3d372713, v15
	v_mul_f32_e32 v19, v15, v19
	v_fma_f32 v19, v15, v19, v15
	v_mul_f32_e32 v19, 0x3f4c422a, v19
	v_add_f32_e32 v19, v19, v19
	v_mul_f32_e32 v19, 0x3fb8aa3b, v19
	v_exp_f32_e32 v19, v19
	v_mul_f32_e32 v15, 0.5, v15
	v_cvt_pk_bf16_f32 v13, v13, v14
	v_cvt_pk_bf16_f32 v14, v20, v17
	v_add_f32_e32 v19, 1.0, v19
	v_rcp_f32_e32 v19, v19
	s_nop 0
	v_add_f32_e32 v19, v19, v19
	v_sub_f32_e32 v19, 1.0, v19
	v_add_f32_e32 v19, 1.0, v19
	v_mul_f32_e32 v15, v15, v19
	v_cvt_pk_bf16_f32 v15, v18, v15
	global_store_dwordx4 v[76:77], v[12:15], off offset:256
	s_nop 1
	v_mul_f32_e32 v12, 0x3d372713, v8
	v_mul_f32_e32 v12, v8, v12
	v_fma_f32 v12, v8, v12, v8
	v_mul_f32_e32 v12, 0x3f4c422a, v12
	v_add_f32_e32 v12, v12, v12
	v_mul_f32_e32 v12, 0x3fb8aa3b, v12
	v_exp_f32_e32 v12, v12
	v_mul_f32_e32 v8, 0.5, v8
	v_add_f32_e32 v12, 1.0, v12
	v_rcp_f32_e32 v12, v12
	s_nop 0
	v_add_f32_e32 v12, v12, v12
	v_sub_f32_e32 v12, 1.0, v12
	v_add_f32_e32 v12, 1.0, v12
	v_mul_f32_e32 v8, v8, v12
	v_mul_f32_e32 v12, 0x3d372713, v4
	v_mul_f32_e32 v12, v4, v12
	v_fma_f32 v12, v4, v12, v4
	v_mul_f32_e32 v12, 0x3f4c422a, v12
	v_add_f32_e32 v12, v12, v12
	v_mul_f32_e32 v12, 0x3fb8aa3b, v12
	v_exp_f32_e32 v12, v12
	v_mul_f32_e32 v4, 0.5, v4
	v_add_f32_e32 v12, 1.0, v12
	v_rcp_f32_e32 v12, v12
	s_nop 0
	v_add_f32_e32 v12, v12, v12
	v_sub_f32_e32 v12, 1.0, v12
	v_add_f32_e32 v12, 1.0, v12
	v_mul_f32_e32 v12, v4, v12
	v_mul_f32_e32 v4, 0x3d372713, v9
	v_mul_f32_e32 v4, v9, v4
	v_fma_f32 v4, v9, v4, v9
	v_mul_f32_e32 v4, 0x3f4c422a, v4
	v_add_f32_e32 v4, v4, v4
	v_mul_f32_e32 v4, 0x3fb8aa3b, v4
	v_exp_f32_e32 v4, v4
	v_mul_f32_e32 v9, 0.5, v9
	v_add_f32_e32 v4, 1.0, v4
	v_rcp_f32_e32 v4, v4
	s_nop 0
	v_add_f32_e32 v4, v4, v4
	v_sub_f32_e32 v4, 1.0, v4
	v_add_f32_e32 v4, 1.0, v4
	v_mul_f32_e32 v4, v9, v4
	v_mul_f32_e32 v9, 0x3d372713, v5
	v_mul_f32_e32 v9, v5, v9
	v_fma_f32 v9, v5, v9, v5
	v_mul_f32_e32 v9, 0x3f4c422a, v9
	v_add_f32_e32 v9, v9, v9
	v_mul_f32_e32 v9, 0x3fb8aa3b, v9
	v_exp_f32_e32 v9, v9
	v_mul_f32_e32 v5, 0.5, v5
	v_cvt_pk_bf16_f32 v4, v8, v4
	v_add_f32_e32 v9, 1.0, v9
	v_rcp_f32_e32 v9, v9
	s_nop 0
	v_add_f32_e32 v9, v9, v9
	v_sub_f32_e32 v9, 1.0, v9
	v_add_f32_e32 v9, 1.0, v9
	v_mul_f32_e32 v9, v5, v9
	v_mul_f32_e32 v5, 0x3d372713, v10
	v_mul_f32_e32 v5, v10, v5
	v_fma_f32 v5, v10, v5, v10
	v_mul_f32_e32 v5, 0x3f4c422a, v5
	v_add_f32_e32 v5, v5, v5
	v_mul_f32_e32 v5, 0x3fb8aa3b, v5
	v_exp_f32_e32 v5, v5
	v_mul_f32_e32 v10, 0.5, v10
	v_add_f32_e32 v5, 1.0, v5
	v_rcp_f32_e32 v5, v5
	s_nop 0
	v_add_f32_e32 v5, v5, v5
	v_sub_f32_e32 v5, 1.0, v5
	v_add_f32_e32 v5, 1.0, v5
	v_mul_f32_e32 v5, v10, v5
	v_mul_f32_e32 v10, 0x3d372713, v6
	v_mul_f32_e32 v10, v6, v10
	v_fma_f32 v10, v6, v10, v6
	v_mul_f32_e32 v10, 0x3f4c422a, v10
	v_add_f32_e32 v10, v10, v10
	v_mul_f32_e32 v10, 0x3fb8aa3b, v10
	v_exp_f32_e32 v10, v10
	v_mul_f32_e32 v6, 0.5, v6
	v_add_f32_e32 v10, 1.0, v10
	v_rcp_f32_e32 v10, v10
	s_nop 0
	v_add_f32_e32 v10, v10, v10
	v_sub_f32_e32 v10, 1.0, v10
	v_add_f32_e32 v10, 1.0, v10
	v_mul_f32_e32 v10, v6, v10
	v_mul_f32_e32 v6, 0x3d372713, v11
	v_mul_f32_e32 v6, v11, v6
	v_fma_f32 v6, v11, v6, v11
	v_mul_f32_e32 v6, 0x3f4c422a, v6
	v_add_f32_e32 v6, v6, v6
	v_mul_f32_e32 v6, 0x3fb8aa3b, v6
	v_exp_f32_e32 v6, v6
	v_mul_f32_e32 v11, 0.5, v11
	v_add_f32_e32 v6, 1.0, v6
	v_rcp_f32_e32 v6, v6
	s_nop 0
	v_add_f32_e32 v6, v6, v6
	v_sub_f32_e32 v6, 1.0, v6
	v_add_f32_e32 v6, 1.0, v6
	v_mul_f32_e32 v6, v11, v6
	v_mul_f32_e32 v11, 0x3d372713, v7
	v_mul_f32_e32 v11, v7, v11
	v_fma_f32 v11, v7, v11, v7
	v_mul_f32_e32 v11, 0x3f4c422a, v11
	v_add_f32_e32 v11, v11, v11
	v_mul_f32_e32 v11, 0x3fb8aa3b, v11
	v_exp_f32_e32 v11, v11
	v_mul_f32_e32 v7, 0.5, v7
	v_cvt_pk_bf16_f32 v5, v5, v6
	v_cvt_pk_bf16_f32 v6, v12, v9
	v_add_f32_e32 v11, 1.0, v11
	s_mov_b64 s[0:1], -1
	v_rcp_f32_e32 v11, v11
	s_nop 0
	v_add_f32_e32 v11, v11, v11
	v_sub_f32_e32 v11, 1.0, v11
	v_add_f32_e32 v11, 1.0, v11
	v_mul_f32_e32 v7, v7, v11
	s_andn2_b64 vcc, exec, s[64:65]
	v_cvt_pk_bf16_f32 v7, v10, v7
	global_store_dwordx4 v[78:79], v[4:7], off offset:256
	s_cbranch_vccnz .LBB0_1176
	s_andn2_b64 vcc, exec, s[52:53]
	s_cbranch_vccnz .LBB0_1175
	s_barrier
	s_branch .LBB0_1175

.LBB0_2805:
	s_lshl_b32 s12, 1, s9
	s_or_b32 s12, s12, s8
	v_cmp_le_u32_e64 s[54:55], s12, v24
	v_cmp_le_u32_e64 s[56:57], s12, v23
	v_cmp_le_u32_e64 s[58:59], s12, v22
	v_cmp_le_u32_e64 s[60:61], s12, v21
	s_bcnt1_i32_b64 s13, s[54:55]
	s_bcnt1_i32_b64 s14, s[56:57]
	s_add_i32 s13, s14, s13
	s_bcnt1_i32_b64 s14, s[58:59]
	s_add_i32 s13, s13, s14
	s_bcnt1_i32_b64 s14, s[60:61]
	s_add_i32 s13, s13, s14
	s_cmp_gt_u32 s13, 7
	s_cselect_b32 s8, s12, s8
	s_cmp_eq_u32 s13, 8
	s_cbranch_scc1 .Lmy_bis_exit
	s_add_i32 s12, s9, -1
	s_lshl_b32 s12, 1, s12
	s_or_b32 s12, s12, s8
	v_cmp_le_u32_e64 s[54:55], s12, v24
	v_cmp_le_u32_e64 s[56:57], s12, v23
	v_cmp_le_u32_e64 s[58:59], s12, v22
	v_cmp_le_u32_e64 s[60:61], s12, v21
	s_bcnt1_i32_b64 s13, s[54:55]
	s_bcnt1_i32_b64 s14, s[56:57]
	s_add_i32 s13, s14, s13
	s_bcnt1_i32_b64 s14, s[58:59]
	s_add_i32 s13, s13, s14
	s_bcnt1_i32_b64 s14, s[60:61]
	s_add_i32 s13, s13, s14
	s_cmp_gt_u32 s13, 7
	s_cselect_b32 s8, s12, s8
	s_cmp_eq_u32 s13, 8
	s_cbranch_scc1 .Lmy_bis_exit
	s_add_i32 s12, s9, -2
	s_lshl_b32 s12, 1, s12
	s_or_b32 s12, s12, s8
	v_cmp_le_u32_e64 s[54:55], s12, v24
	v_cmp_le_u32_e64 s[56:57], s12, v23
	v_cmp_le_u32_e64 s[58:59], s12, v22
	v_cmp_le_u32_e64 s[60:61], s12, v21
	s_bcnt1_i32_b64 s13, s[54:55]
	s_bcnt1_i32_b64 s14, s[56:57]
	s_add_i32 s13, s14, s13
	s_bcnt1_i32_b64 s14, s[58:59]
	s_add_i32 s13, s13, s14
	s_bcnt1_i32_b64 s14, s[60:61]
	s_add_i32 s13, s13, s14
	s_cmp_gt_u32 s13, 7
	s_cselect_b32 s8, s12, s8
	s_cmp_eq_u32 s13, 8
	s_cbranch_scc1 .Lmy_bis_exit
	s_add_i32 s9, s9, -3
	s_lshl_b32 s12, 1, s9
	s_or_b32 s12, s12, s8
	v_cmp_le_u32_e64 s[54:55], s12, v24
	v_cmp_le_u32_e64 s[56:57], s12, v23
	v_cmp_le_u32_e64 s[58:59], s12, v22
	v_cmp_le_u32_e64 s[60:61], s12, v21
	s_bcnt1_i32_b64 s13, s[54:55]
	s_bcnt1_i32_b64 s14, s[56:57]
	s_add_i32 s13, s14, s13
	s_bcnt1_i32_b64 s14, s[58:59]
	s_add_i32 s13, s13, s14
	s_bcnt1_i32_b64 s14, s[60:61]
	s_add_i32 s13, s13, s14
	s_cmp_gt_u32 s13, 7
	s_cselect_b32 s8, s12, s8
	s_cmp_eq_u32 s13, 8
	s_cbranch_scc1 .Lmy_bis_exit
	v_sub_co_u32_e64 v25, s[12:13], s9, 1
	s_nop 0
	v_readfirstlane_b32 s9, v25
	s_and_b64 vcc, exec, s[12:13]
	s_cbranch_vccz .LBB0_2805
	s_branch .Lmy_bis_done
